# MLA loop as a depth-3 software pipeline: P.V of tile k-2 and QK of tile k interleaved uniformly with the softmax front half of tile k-1 (single packed-P buffer), scalar instead of packed f32 VALU, sho
# speedup vs baseline: 1.0309x; 1.0112x over previous
.LBB0_1010:
	s_lshr_b32 s4, s94, 1
	s_mul_i32 s4, s4, s82
	v_readlane_b32 s5, v236, 34
	s_add_i32 s5, s4, s5
	s_and_b32 s4, s5, 7
	s_ashr_i32 s6, s5, 5
	s_lshl_b32 s5, s5, 5
	s_and_b32 s6, s6, -8
	s_and_b32 s5, s5, 0x1f00
	s_or_b32 s4, s6, s4
	s_and_b32 s6, s94, 1
	s_xor_b32 s7, s5, 0x3f00
	v_readlane_b32 s12, v237, 61
	s_cmp_eq_u32 s6, 0
	v_readlane_b32 s13, v237, 62
	v_readlane_b32 s14, v237, 63
	v_readlane_b32 s15, v238, 0
	v_readlane_b32 s16, v238, 1
	v_readlane_b32 s17, v238, 2
	v_readlane_b32 s18, v238, 3
	v_readlane_b32 s19, v238, 4
	v_readlane_b32 s20, v238, 5
	v_readlane_b32 s21, v238, 6
	v_readlane_b32 s22, v238, 7
	v_readlane_b32 s23, v238, 8
	s_cselect_b32 s8, s5, s7
	v_readlane_b32 s24, v238, 9
	v_readlane_b32 s25, v238, 10
	v_readlane_b32 s26, v238, 11
	v_readlane_b32 s27, v238, 12
	s_mov_b64 s[12:13], s[16:17]
	s_lshl_b32 s97, s8, 11
	s_mov_b64 s[14:15], s[18:19]
	s_mov_b64 s[16:17], s[20:21]
	s_mov_b64 s[18:19], s[22:23]
	s_add_u32 s5, s18, s97
	s_addc_u32 s6, s19, 0
	s_lshl_b32 s66, s4, 7
	s_ashr_i32 s67, s66, 31
	s_add_u32 s9, s5, s66
	s_mov_b64 s[20:21], s[24:25]
	s_addc_u32 s10, s6, s67
	s_lshl_b32 s5, s8, 10
	s_add_u32 s5, s20, s5
	s_addc_u32 s6, s21, 0
	s_lshl_b32 s7, s4, 6
	s_ashr_i32 s11, s7, 31
	s_add_u32 s12, s5, s7
	s_mov_b64 s[22:23], s[26:27]
	s_addc_u32 s11, s6, s11
	s_add_u32 s6, s22, s66
	s_addc_u32 s7, s23, s67
	s_ashr_i32 s5, s4, 31
	s_lshl_b64 s[4:5], s[4:5], 21
	s_add_u32 s4, s84, s4
	v_readfirstlane_b32 s13, v0
	s_addc_u32 s5, s85, s5
	s_lshr_b32 s14, s13, 6
	s_lshl_b32 s70, s14, 5
	s_lshr_b32 s72, s8, 6
	s_add_i32 s95, s70, s8
	s_and_b32 s8, s13, 0x3fffffc0
	s_lshl_b32 s8, s8, 2
	s_add_i32 s8, s8, 0
	s_add_i32 s13, s8, 0x14000
	s_add_i32 s72, s72, 4
	s_lshl_b32 s74, s14, 10
	s_cmp_lg_u32 0, -1
	s_cselect_b32 s8, 0, 0
	s_add_i32 s73, s74, s8
	s_cmp_lg_u32 s81, -1
	s_cselect_b32 s8, s81, 0
	v_or_b32_e32 v6, s74, v206
	s_add_i32 s74, s74, s8
	s_add_i32 s75, s74, 0x8000
	s_lshl_b64 s[92:93], s[70:71], 11
	s_add_u32 s8, s9, s92
	s_addc_u32 s9, s10, s93
	v_lshl_add_u64 v[8:9], s[8:9], 0, v[158:159]
	s_lshl_b64 s[8:9], s[70:71], 10
	s_add_u32 s8, s12, s8
	s_addc_u32 s9, s11, s9
	v_lshl_add_u64 v[8:9], v[8:9], 0, v[160:161]
	v_lshl_add_u64 v[10:11], s[8:9], 0, v[162:163]
	v_lshl_add_u64 v[10:11], v[10:11], 0, v[160:161]
	global_load_dwordx4 v[100:103], v[8:9], off
	global_load_dwordx4 v[104:107], v[8:9], off offset:32
	global_load_dwordx4 v[108:111], v[8:9], off offset:64
	global_load_dwordx4 v[112:115], v[8:9], off offset:96
	global_load_dwordx4 v[116:119], v[10:11], off
	global_load_dwordx4 v[120:123], v[10:11], off offset:32
	v_lshl_or_b32 v4, s14, 3, v205
	v_lshrrev_b32_e32 v2, 1, v4
	v_xor_b32_e32 v2, v2, v0
	v_lshlrev_b32_e32 v2, 4, v2
	v_and_b32_e32 v5, 0x70, v2
	v_lshl_or_b32 v2, v4, 11, v5
	v_lshl_or_b32 v4, v4, 7, v5
	v_lshl_add_u64 v[8:9], s[6:7], 0, v[2:3]
	s_mov_b32 s6, m0
	s_mov_b32 m0, s74
	s_nop 0
	global_load_lds_dwordx4 v[8:9], off
	s_mov_b32 m0, s6
	v_mov_b32_e32 v5, v3
	v_lshl_add_u64 v[4:5], s[16:17], 0, v[4:5]
	s_mov_b32 s6, m0
	s_mov_b32 m0, s75
	s_nop 0
	global_load_lds_dwordx4 v[4:5], off
	s_mov_b32 m0, s6
	v_mov_b32_e32 v7, v3
	v_lshl_add_u64 v[6:7], s[4:5], 0, v[6:7]
	s_mov_b32 s4, m0
	s_mov_b32 m0, s73
	s_nop 0
	global_load_lds_dwordx4 v[6:7], off
	s_mov_b32 m0, s4
	v_mov_b32_e32 v16, v3
	v_mov_b32_e32 v17, v3
	s_waitcnt vmcnt(0) lgkmcnt(0)
	s_barrier
	v_lshl_add_u64 v[194:195], v[8:9], 0, s[88:89]
	v_lshl_add_u64 v[196:197], v[4:5], 0, s[68:69]
	v_lshl_add_u64 v[198:199], v[6:7], 0, s[68:69]
	v_mov_b32_e32 v2, v3
	v_mov_b32_e32 v4, v3
	v_mov_b32_e32 v5, v3
	v_mov_b32_e32 v6, v3
	v_mov_b32_e32 v7, v3
	v_mov_b32_e32 v8, v3
	v_mov_b32_e32 v9, v3
	v_mov_b32_e32 v10, v3
	v_mov_b32_e32 v11, v3
	v_mov_b32_e32 v12, v3
	v_mov_b32_e32 v13, v3
	v_mov_b32_e32 v14, v3
	v_mov_b32_e32 v15, v3
	v_mov_b64_e32 v[66:67], v[16:17]
	v_mov_b64_e32 v[50:51], v[16:17]
	v_mov_b64_e32 v[34:35], v[16:17]
	v_mov_b64_e32 v[64:65], v[14:15]
	v_mov_b64_e32 v[62:63], v[12:13]
	v_mov_b64_e32 v[60:61], v[10:11]
	v_mov_b64_e32 v[58:59], v[8:9]
	v_mov_b64_e32 v[56:57], v[6:7]
	v_mov_b64_e32 v[54:55], v[4:5]
	v_mov_b64_e32 v[52:53], v[2:3]
	v_mov_b64_e32 v[48:49], v[14:15]
	v_mov_b64_e32 v[46:47], v[12:13]
	v_mov_b64_e32 v[44:45], v[10:11]
	v_mov_b64_e32 v[42:43], v[8:9]
	v_mov_b64_e32 v[40:41], v[6:7]
	v_mov_b64_e32 v[38:39], v[4:5]
	v_mov_b64_e32 v[36:37], v[2:3]
	v_mov_b64_e32 v[32:33], v[14:15]
	v_mov_b64_e32 v[30:31], v[12:13]
	v_mov_b64_e32 v[28:29], v[10:11]
	v_mov_b64_e32 v[26:27], v[8:9]
	v_mov_b64_e32 v[24:25], v[6:7]
	v_mov_b64_e32 v[22:23], v[4:5]
	v_mov_b64_e32 v[20:21], v[2:3]
	v_mov_b64_e32 v[18:19], v[16:17]
	s_or_b32 s70, s95, 31
	v_lshl_add_u32 v214, v156, 2, s13
	v_lshl_add_u32 v213, v204, 2, s13
	v_add_u32_e32 v215, s95, v209
	v_mov_b32_e32 v216, 0xf149f2ca
	s_mov_b32 s76, 63
	v_mov_b64_e32 v[16:17], v[14:15]
	v_mov_b64_e32 v[14:15], v[12:13]
	v_mov_b64_e32 v[12:13], v[10:11]
	v_mov_b64_e32 v[10:11], v[8:9]
	v_mov_b64_e32 v[8:9], v[6:7]
	v_mov_b64_e32 v[6:7], v[4:5]
	v_mov_b64_e32 v[4:5], v[2:3]
	s_mov_b32 s77, 0
	v_mov_b32_e32 v2, 0
	s_mov_b32 s40, m0
	s_lshr_b32 s4, s70, 6
	s_add_i32 s4, s4, 1
	s_min_u32 s42, s4, s72
	s_lshr_b32 s43, s95, 6
	v_add_u32_e32 v242, 0x10000, v200
	v_add_u32_e32 v243, 0x10000, v201
	v_readlane_b32 s37, v236, 34
	v_readfirstlane_b32 s4, v0
	s_nop 3
	s_lshr_b32 s36, s4, 6
	s_lshr_b32 s5, s37, 6
	s_lshl_b32 s5, s5, 7
	s_lshl_b32 s6, s36, 4
	s_add_i32 s5, s5, s6
	s_and_b32 s7, s37, 63
	s_lshl_b32 s8, s5, 14
	s_lshl_b32 s9, s7, 8
	s_add_i32 s8, s8, s9
	v_readlane_b32 s52, v237, 29
	v_readlane_b32 s53, v237, 30
	s_add_u32 s52, s52, s8
	s_addc_u32 s53, s53, 0
	s_bfe_u32 s8, s7, 0x40001
	s_lshl_b32 s8, s8, 8
	s_and_b32 s9, s7, 1
	s_lshl_b32 s9, s9, 6
	s_add_i32 s8, s8, s9
	s_lshr_b32 s9, s7, 5
	s_lshl_b32 s9, s9, 7
	s_add_i32 s8, s8, s9
	s_lshl_b32 s8, s8, 11
	s_add_i32 s8, s8, s5
	v_readlane_b32 s54, v237, 51
	v_readlane_b32 s55, v237, 52
	s_add_u32 s54, s54, s8
	s_addc_u32 s55, s55, 0
	s_lshr_b32 s5, s37, 5
	s_lshl_b32 s5, s5, 7
	s_add_i32 s5, s5, s6
	s_and_b32 s7, s37, 31
	s_lshl_b32 s8, s5, 13
	s_lshl_b32 s9, s7, 8
	s_add_i32 s8, s8, s9
	v_readlane_b32 s58, v237, 33
	v_readlane_b32 s59, v237, 34
	s_add_u32 s58, s58, s8
	s_addc_u32 s59, s59, 0
	s_lshl_b32 s8, s7, 17
	s_add_i32 s8, s8, s5
	v_readlane_b32 s60, v237, 53
	v_readlane_b32 s61, v237, 54
	s_add_u32 s60, s60, s8
	s_addc_u32 s61, s61, 0
	s_mov_b32 s50, 0x44000000
	s_mov_b32 s51, 0x44000000
	s_mov_b32 s47, 0
	s_mov_b32 s48, 0
	v_and_b32_e32 v241, 63, v0
	v_lshlrev_b32_e32 v240, 11, v241
	v_lshlrev_b32_e32 v241, 2, v241
	v_mov_b32_e32 v217, 1.0
	s_cmp_ge_u32 s36, 4
	s_cbranch_scc1 .Lm_Lstart

.Lm_nd1:
	ds_read_b128 v[166:169], v200 offset:32768
	ds_read_b128 v[170:173], v201 offset:32768
	ds_read_b128 v[174:177], v200 offset:36864
	ds_read_b128 v[178:181], v201 offset:36864
	ds_read_b128 v[182:185], v202 offset:32768
	ds_read_b128 v[186:189], v203 offset:32768
	ds_read_b128 v[218:221], v202 offset:36864
	ds_read_b128 v[222:225], v203 offset:36864
	s_waitcnt lgkmcnt(6)
	v_mfma_f32_32x32x64_f8f6f4 v[68:83], v[166:173], v[100:107], 0
	ds_read_b128 v[166:169], v242 offset:0
	ds_read_b128 v[170:173], v243 offset:0
	s_waitcnt lgkmcnt(6)
	v_mfma_f32_32x32x64_f8f6f4 v[84:99], v[174:181], v[100:107], 0
	ds_read_b128 v[174:177], v242 offset:4096
	ds_read_b128 v[178:181], v243 offset:4096
	s_waitcnt lgkmcnt(6)
	v_mfma_f32_32x32x64_f8f6f4 v[68:83], v[182:189], v[108:115], v[68:83]
	s_waitcnt lgkmcnt(4)
	v_mfma_f32_32x32x64_f8f6f4 v[84:99], v[218:225], v[108:115], v[84:99]
	s_waitcnt lgkmcnt(2)
	v_mfma_f32_32x32x64_f8f6f4 v[68:83], v[166:173], v[116:123], v[68:83]
	s_waitcnt lgkmcnt(0)
	v_mfma_f32_32x32x64_f8f6f4 v[84:99], v[174:181], v[116:123], v[84:99]
	s_waitcnt vmcnt(0) lgkmcnt(0)
	s_cmp_eq_u32 s48, 0
	s_cbranch_scc1 .Lm_bf3
	v_pk_mul_f32 v[226:227], v[226:227], s[50:51]
	v_pk_mul_f32 v[228:229], v[228:229], s[50:51]
	v_pk_mul_f32 v[230:231], v[230:231], s[50:51]
	v_pk_mul_f32 v[232:233], v[232:233], s[50:51]
	v_med3_f32 v226, v226, s33, v212
	v_med3_f32 v227, v227, s33, v212
	v_med3_f32 v228, v228, s33, v212
	v_med3_f32 v229, v229, s33, v212
	v_med3_f32 v230, v230, s33, v212
	v_med3_f32 v231, v231, s33, v212
	v_med3_f32 v232, v232, s33, v212
	v_med3_f32 v233, v233, s33, v212
	v_cvt_pk_fp8_f32 v246, v226, v227
	v_cvt_pk_fp8_f32 v247, v230, v231
	v_cvt_pk_fp8_f32 v246, v228, v229 op_sel:[0,0,1]
	v_cvt_pk_fp8_f32 v247, v232, v233 op_sel:[0,0,1]
	global_store_dwordx4 v240, v[244:247], s[44:45]
	s_mov_b32 s48, 0

.Lm_bs2:
	s_barrier
	s_add_i32 s77, s77, 1
	v_subrev_u32_e32 v215, 64, v215
	v_lshl_add_u64 v[194:195], v[194:195], 0, s[88:89]
	v_lshl_add_u64 v[196:197], v[196:197], 0, s[68:69]
	v_lshl_add_u64 v[198:199], v[198:199], 0, s[68:69]
	s_add_i32 s4, s77, 1
	s_cmp_ge_u32 s4, s72
	s_cbranch_scc1 .Lm_nd5
	s_add_i32 m0, s74, 0x2000
	s_add_i32 s8, s75, 0x8000
	global_load_lds_dwordx4 v[194:195], off
	s_mov_b32 m0, s8
	s_add_i32 s8, s73, 0x2000
	global_load_lds_dwordx4 v[196:197], off
	s_mov_b32 m0, s8
	s_nop 0
	global_load_lds_dwordx4 v[198:199], off

.Lm_nm7:
	v_max3_f32 v239, v68, v69, v70
	v_max3_f32 v235, v84, v85, v86
	v_max3_f32 v239, v239, v71, v72
	v_max3_f32 v235, v235, v87, v88
	v_max3_f32 v239, v239, v73, v74
	v_max3_f32 v235, v235, v89, v90
	v_max3_f32 v239, v239, v75, v76
	v_max3_f32 v235, v235, v91, v92
	v_max3_f32 v239, v239, v77, v78
	v_max3_f32 v235, v235, v93, v94
	v_max3_f32 v239, v239, v79, v80
	v_max3_f32 v235, v235, v95, v96
	v_max3_f32 v239, v239, v81, v82
	v_max3_f32 v235, v235, v97, v98
	v_max3_f32 v239, v239, v83, v99
	v_max_f32_e32 v239, v239, v235
	v_mov_b32_e32 v234, v239
	s_nop 1
	v_permlane32_swap_b32_e32 v239, v234
	v_max_f32_e32 v239, v239, v234
	v_sub_f32_e32 v235, v239, v216
	v_mul_f32_e32 v235, 0x3a93cd3a, v235
	v_cmp_ge_f32_e32 vcc, 2.0, v235
	s_cmp_eq_u64 vcc, exec
	s_cbranch_scc1 .Lm_nr8
	v_max_f32_e32 v235, v216, v239
	v_sub_f32_e32 v217, v216, v235
	v_mul_f32_e32 v217, 0x3ad53b94, v217
	v_exp_f32_e32 v217, v217
	v_mov_b32_e32 v216, v235
	s_and_saveexec_b64 s[6:7], s[0:1]
	ds_write_b32 v214, v217 offset:128
	s_or_b64 exec, exec, s[6:7]
	s_waitcnt lgkmcnt(0)
	ds_read_b128 v[140:143], v213 offset:128
	s_waitcnt lgkmcnt(0)
	v_pk_mul_f32 v[52:53], v[52:53], v[140:141]
	v_pk_mul_f32 v[54:55], v[54:55], v[142:143]
	v_pk_mul_f32 v[36:37], v[36:37], v[140:141]
	v_pk_mul_f32 v[38:39], v[38:39], v[142:143]
	v_pk_mul_f32 v[20:21], v[20:21], v[140:141]
	v_pk_mul_f32 v[22:23], v[22:23], v[142:143]
	v_pk_mul_f32 v[4:5], v[4:5], v[140:141]
	v_pk_mul_f32 v[6:7], v[6:7], v[142:143]
	ds_read_b128 v[140:143], v213 offset:160
	s_waitcnt lgkmcnt(0)
	v_pk_mul_f32 v[56:57], v[56:57], v[140:141]
	v_pk_mul_f32 v[58:59], v[58:59], v[142:143]
	v_pk_mul_f32 v[40:41], v[40:41], v[140:141]
	v_pk_mul_f32 v[42:43], v[42:43], v[142:143]
	v_pk_mul_f32 v[24:25], v[24:25], v[140:141]
	v_pk_mul_f32 v[26:27], v[26:27], v[142:143]
	v_pk_mul_f32 v[8:9], v[8:9], v[140:141]
	v_pk_mul_f32 v[10:11], v[10:11], v[142:143]
	ds_read_b128 v[140:143], v213 offset:192
	s_waitcnt lgkmcnt(0)
	v_pk_mul_f32 v[60:61], v[60:61], v[140:141]
	v_pk_mul_f32 v[62:63], v[62:63], v[142:143]
	v_pk_mul_f32 v[44:45], v[44:45], v[140:141]
	v_pk_mul_f32 v[46:47], v[46:47], v[142:143]
	v_pk_mul_f32 v[28:29], v[28:29], v[140:141]
	v_pk_mul_f32 v[30:31], v[30:31], v[142:143]
	v_pk_mul_f32 v[12:13], v[12:13], v[140:141]
	v_pk_mul_f32 v[14:15], v[14:15], v[142:143]
	ds_read_b128 v[140:143], v213 offset:224
	s_waitcnt lgkmcnt(0)
	v_pk_mul_f32 v[64:65], v[64:65], v[140:141]
	v_pk_mul_f32 v[66:67], v[66:67], v[142:143]
	v_pk_mul_f32 v[48:49], v[48:49], v[140:141]
	v_pk_mul_f32 v[50:51], v[50:51], v[142:143]
	v_pk_mul_f32 v[32:33], v[32:33], v[140:141]
	v_pk_mul_f32 v[34:35], v[34:35], v[142:143]
	v_pk_mul_f32 v[16:17], v[16:17], v[140:141]
	v_pk_mul_f32 v[18:19], v[18:19], v[142:143]
.Lm_nr8:
	v_fmamk_f32 v190, v216, 0xbad53b94, v210
	v_fma_f32 v68, v68, s96, v190
	v_fma_f32 v69, v69, s96, v190
	v_fma_f32 v84, v84, s96, v190
	v_fma_f32 v85, v85, s96, v190
	v_fma_f32 v70, v70, s96, v190
	v_fma_f32 v71, v71, s96, v190
	v_fma_f32 v86, v86, s96, v190
	v_fma_f32 v87, v87, s96, v190
	v_fma_f32 v72, v72, s96, v190
	v_fma_f32 v73, v73, s96, v190
	v_fma_f32 v88, v88, s96, v190
	v_fma_f32 v89, v89, s96, v190
	v_fma_f32 v74, v74, s96, v190
	v_fma_f32 v75, v75, s96, v190
	v_fma_f32 v90, v90, s96, v190
	v_fma_f32 v91, v91, s96, v190
	v_fma_f32 v76, v76, s96, v190
	v_fma_f32 v77, v77, s96, v190
	v_fma_f32 v92, v92, s96, v190
	v_fma_f32 v93, v93, s96, v190
	v_fma_f32 v78, v78, s96, v190
	v_fma_f32 v79, v79, s96, v190
	v_fma_f32 v94, v94, s96, v190
	v_fma_f32 v95, v95, s96, v190
	v_fma_f32 v80, v80, s96, v190
	v_fma_f32 v81, v81, s96, v190
	v_fma_f32 v96, v96, s96, v190
	v_fma_f32 v97, v97, s96, v190
	v_fma_f32 v82, v82, s96, v190
	v_fma_f32 v83, v83, s96, v190
	v_fma_f32 v98, v98, s96, v190
	v_fma_f32 v99, v99, s96, v190
	v_exp_f32_e32 v68, v68
	v_exp_f32_e32 v69, v69
	v_exp_f32_e32 v70, v70
	v_exp_f32_e32 v71, v71
	v_exp_f32_e32 v72, v72
	v_exp_f32_e32 v73, v73
	v_exp_f32_e32 v74, v74
	v_exp_f32_e32 v75, v75
	v_exp_f32_e32 v76, v76
	v_exp_f32_e32 v77, v77
	v_exp_f32_e32 v78, v78
	v_exp_f32_e32 v79, v79
	v_exp_f32_e32 v80, v80
	v_exp_f32_e32 v81, v81
	v_exp_f32_e32 v82, v82
	v_exp_f32_e32 v83, v83
	v_exp_f32_e32 v84, v84
	v_exp_f32_e32 v85, v85
	v_exp_f32_e32 v86, v86
	v_exp_f32_e32 v87, v87
	v_exp_f32_e32 v88, v88
	v_exp_f32_e32 v89, v89
	v_exp_f32_e32 v90, v90
	v_exp_f32_e32 v91, v91
	v_exp_f32_e32 v92, v92
	v_exp_f32_e32 v93, v93
	v_exp_f32_e32 v94, v94
	v_exp_f32_e32 v95, v95
	v_exp_f32_e32 v96, v96
	v_exp_f32_e32 v97, v97
	v_exp_f32_e32 v98, v98
	v_exp_f32_e32 v99, v99
	ds_read_b128 v[166:169], v200 offset:49152
	ds_read_b128 v[170:173], v201 offset:49152
	ds_read_b128 v[174:177], v200 offset:53248
	ds_read_b128 v[178:181], v201 offset:53248
	ds_read_b128 v[182:185], v202 offset:49152
	ds_read_b128 v[186:189], v203 offset:49152
	ds_read_b128 v[218:221], v202 offset:53248
	ds_read_b128 v[222:225], v203 offset:53248
	s_waitcnt lgkmcnt(6)
	v_mfma_f32_32x32x64_f8f6f4 v[124:139], v[166:173], v[100:107], 0
	ds_read_b128 v[166:169], v242 offset:8192
	ds_read_b128 v[170:173], v243 offset:8192
	s_waitcnt lgkmcnt(6)
	v_mfma_f32_32x32x64_f8f6f4 v[140:155], v[174:181], v[100:107], 0
	ds_read_b128 v[174:177], v242 offset:12288
	ds_read_b128 v[178:181], v243 offset:12288
	s_waitcnt lgkmcnt(6)
	v_mfma_f32_32x32x64_f8f6f4 v[124:139], v[182:189], v[108:115], v[124:139]
	s_waitcnt lgkmcnt(4)
	v_mfma_f32_32x32x64_f8f6f4 v[140:155], v[218:225], v[108:115], v[140:155]
	s_waitcnt lgkmcnt(2)
	v_mfma_f32_32x32x64_f8f6f4 v[124:139], v[166:173], v[116:123], v[124:139]
	s_waitcnt lgkmcnt(0)
	v_mfma_f32_32x32x64_f8f6f4 v[140:155], v[174:181], v[116:123], v[140:155]
	s_branch .Lm_p1e6
.Lm_p1s6:
	s_cmp_le_u32 s77, s43
	s_cbranch_scc1 .Lm_nm9
	v_add_u32_e32 v239, 64, v215
	v_cmp_gt_i32_e64 s[4:5], 0, v239
	v_cmp_gt_i32_e64 s[6:7], 1, v239
	v_cmp_gt_i32_e64 s[8:9], 2, v239
	v_cmp_gt_i32_e64 s[10:11], 3, v239
	v_cndmask_b32_e64 v68, v68, v211, s[4:5]
	v_cndmask_b32_e64 v69, v69, v211, s[6:7]
	v_cndmask_b32_e64 v70, v70, v211, s[8:9]
	v_cndmask_b32_e64 v71, v71, v211, s[10:11]
	v_cmp_gt_i32_e64 s[4:5], 8, v239
	v_cmp_gt_i32_e64 s[6:7], 9, v239
	v_cmp_gt_i32_e64 s[8:9], 10, v239
	v_cmp_gt_i32_e64 s[10:11], 11, v239
	v_cndmask_b32_e64 v72, v72, v211, s[4:5]
	v_cndmask_b32_e64 v73, v73, v211, s[6:7]
	v_cndmask_b32_e64 v74, v74, v211, s[8:9]
	v_cndmask_b32_e64 v75, v75, v211, s[10:11]
	v_cmp_gt_i32_e64 s[4:5], 16, v239
	v_cmp_gt_i32_e64 s[6:7], 17, v239
	v_cmp_gt_i32_e64 s[8:9], 18, v239
	v_cmp_gt_i32_e64 s[10:11], 19, v239
	v_cndmask_b32_e64 v76, v76, v211, s[4:5]
	v_cndmask_b32_e64 v77, v77, v211, s[6:7]
	v_cndmask_b32_e64 v78, v78, v211, s[8:9]
	v_cndmask_b32_e64 v79, v79, v211, s[10:11]
	v_cmp_gt_i32_e64 s[4:5], 24, v239
	v_cmp_gt_i32_e64 s[6:7], 25, v239
	v_cmp_gt_i32_e64 s[8:9], 26, v239
	v_cmp_gt_i32_e64 s[10:11], 27, v239
	v_cndmask_b32_e64 v80, v80, v211, s[4:5]
	v_cndmask_b32_e64 v81, v81, v211, s[6:7]
	v_cndmask_b32_e64 v82, v82, v211, s[8:9]
	v_cndmask_b32_e64 v83, v83, v211, s[10:11]
	v_cmp_gt_i32_e64 s[4:5], 32, v239
	v_cmp_gt_i32_e64 s[6:7], 33, v239
	v_cmp_gt_i32_e64 s[8:9], 34, v239
	v_cmp_gt_i32_e64 s[10:11], 35, v239
	v_cndmask_b32_e64 v84, v84, v211, s[4:5]
	v_cndmask_b32_e64 v85, v85, v211, s[6:7]
	v_cndmask_b32_e64 v86, v86, v211, s[8:9]
	v_cndmask_b32_e64 v87, v87, v211, s[10:11]
	v_cmp_gt_i32_e64 s[4:5], 40, v239
	v_cmp_gt_i32_e64 s[6:7], 41, v239
	v_cmp_gt_i32_e64 s[8:9], 42, v239
	v_cmp_gt_i32_e64 s[10:11], 43, v239
	v_cndmask_b32_e64 v88, v88, v211, s[4:5]
	v_cndmask_b32_e64 v89, v89, v211, s[6:7]
	v_cndmask_b32_e64 v90, v90, v211, s[8:9]
	v_cndmask_b32_e64 v91, v91, v211, s[10:11]
	v_cmp_gt_i32_e64 s[4:5], 48, v239
	v_cmp_gt_i32_e64 s[6:7], 49, v239
	v_cmp_gt_i32_e64 s[8:9], 50, v239
	v_cmp_gt_i32_e64 s[10:11], 51, v239
	v_cndmask_b32_e64 v92, v92, v211, s[4:5]
	v_cndmask_b32_e64 v93, v93, v211, s[6:7]
	v_cndmask_b32_e64 v94, v94, v211, s[8:9]
	v_cndmask_b32_e64 v95, v95, v211, s[10:11]
	v_cmp_gt_i32_e64 s[4:5], 56, v239
	v_cmp_gt_i32_e64 s[6:7], 57, v239
	v_cmp_gt_i32_e64 s[8:9], 58, v239
	v_cmp_gt_i32_e64 s[10:11], 59, v239
	v_cndmask_b32_e64 v96, v96, v211, s[4:5]
	v_cndmask_b32_e64 v97, v97, v211, s[6:7]
	v_cndmask_b32_e64 v98, v98, v211, s[8:9]
	v_cndmask_b32_e64 v99, v99, v211, s[10:11]

.Lm_nr10:
	v_fmamk_f32 v190, v216, 0xbad53b94, v210
	v_fma_f32 v68, v68, s96, v190
	v_fma_f32 v69, v69, s96, v190
	v_fma_f32 v84, v84, s96, v190
	v_fma_f32 v85, v85, s96, v190
	v_fma_f32 v70, v70, s96, v190
	v_fma_f32 v71, v71, s96, v190
	v_fma_f32 v86, v86, s96, v190
	v_fma_f32 v87, v87, s96, v190
	v_fma_f32 v72, v72, s96, v190
	v_fma_f32 v73, v73, s96, v190
	v_fma_f32 v88, v88, s96, v190
	v_fma_f32 v89, v89, s96, v190
	v_fma_f32 v74, v74, s96, v190
	v_fma_f32 v75, v75, s96, v190
	v_fma_f32 v90, v90, s96, v190
	v_fma_f32 v91, v91, s96, v190
	v_fma_f32 v76, v76, s96, v190
	v_fma_f32 v77, v77, s96, v190
	v_fma_f32 v92, v92, s96, v190
	v_fma_f32 v93, v93, s96, v190
	v_fma_f32 v78, v78, s96, v190
	v_fma_f32 v79, v79, s96, v190
	v_fma_f32 v94, v94, s96, v190
	v_fma_f32 v95, v95, s96, v190
	v_fma_f32 v80, v80, s96, v190
	v_fma_f32 v81, v81, s96, v190
	v_fma_f32 v96, v96, s96, v190
	v_fma_f32 v97, v97, s96, v190
	v_fma_f32 v82, v82, s96, v190
	v_fma_f32 v83, v83, s96, v190
	v_fma_f32 v98, v98, s96, v190
	v_fma_f32 v99, v99, s96, v190
	v_exp_f32_e32 v68, v68
	v_exp_f32_e32 v69, v69
	v_exp_f32_e32 v70, v70
	v_exp_f32_e32 v71, v71
	v_exp_f32_e32 v72, v72
	v_exp_f32_e32 v73, v73
	v_exp_f32_e32 v74, v74
	v_exp_f32_e32 v75, v75
	v_exp_f32_e32 v76, v76
	v_exp_f32_e32 v77, v77
	v_exp_f32_e32 v78, v78
	v_exp_f32_e32 v79, v79
	v_exp_f32_e32 v80, v80
	v_exp_f32_e32 v81, v81
	v_exp_f32_e32 v82, v82
	v_exp_f32_e32 v83, v83
	v_exp_f32_e32 v84, v84
	v_exp_f32_e32 v85, v85
	v_exp_f32_e32 v86, v86
	v_exp_f32_e32 v87, v87
	v_exp_f32_e32 v88, v88
	v_exp_f32_e32 v89, v89
	v_exp_f32_e32 v90, v90
	v_exp_f32_e32 v91, v91
	v_exp_f32_e32 v92, v92
	v_exp_f32_e32 v93, v93
	v_exp_f32_e32 v94, v94
	v_exp_f32_e32 v95, v95
	v_exp_f32_e32 v96, v96
	v_exp_f32_e32 v97, v97
	v_exp_f32_e32 v98, v98
	v_exp_f32_e32 v99, v99
.Lm_p1e6:
	v_add_f32_e32 v192, v68, v70
	v_add_f32_e32 v193, v69, v71
	v_add_f32_e32 v234, v84, v86
	v_add_f32_e32 v235, v85, v87
	v_add_f32_e32 v192, v72, v192
	v_add_f32_e32 v193, v73, v193
	v_cvt_pk_fp8_f32 v248, v68, v69
	v_add_f32_e32 v234, v88, v234
	v_add_f32_e32 v235, v89, v235
	v_cvt_pk_fp8_f32 v249, v72, v73
	v_add_f32_e32 v192, v74, v192
	v_add_f32_e32 v193, v75, v193
	v_cvt_pk_fp8_f32 v250, v76, v77
	v_add_f32_e32 v234, v90, v234
	v_add_f32_e32 v235, v91, v235
	v_cvt_pk_fp8_f32 v251, v80, v81
	v_add_f32_e32 v192, v76, v192
	v_add_f32_e32 v193, v77, v193
	v_cvt_pk_fp8_f32 v252, v84, v85
	v_add_f32_e32 v234, v92, v234
	v_add_f32_e32 v235, v93, v235
	v_cvt_pk_fp8_f32 v253, v88, v89
	v_add_f32_e32 v192, v78, v192
	v_add_f32_e32 v193, v79, v193
	v_cvt_pk_fp8_f32 v254, v92, v93
	v_add_f32_e32 v234, v94, v234
	v_add_f32_e32 v235, v95, v235
	v_cvt_pk_fp8_f32 v255, v96, v97
	v_add_f32_e32 v192, v80, v192
	v_add_f32_e32 v193, v81, v193
	v_add_f32_e32 v234, v96, v234
	v_add_f32_e32 v235, v97, v235
	v_add_f32_e32 v192, v82, v192
	v_add_f32_e32 v193, v83, v193
	v_add_f32_e32 v234, v98, v234
	v_add_f32_e32 v235, v99, v235
	v_add_f32_e32 v192, v192, v234
	v_add_f32_e32 v193, v193, v235
	v_cvt_pk_fp8_f32 v248, v70, v71 op_sel:[0,0,1]
	v_cvt_pk_fp8_f32 v249, v74, v75 op_sel:[0,0,1]
	v_cvt_pk_fp8_f32 v250, v78, v79 op_sel:[0,0,1]
	v_cvt_pk_fp8_f32 v251, v82, v83 op_sel:[0,0,1]
	v_add_f32_e32 v239, v192, v193
	v_cvt_pk_fp8_f32 v252, v86, v87 op_sel:[0,0,1]
	v_cvt_pk_fp8_f32 v253, v90, v91 op_sel:[0,0,1]
	v_mov_b32_e32 v235, v239
	v_cvt_pk_fp8_f32 v254, v94, v95 op_sel:[0,0,1]
	v_cvt_pk_fp8_f32 v255, v98, v99 op_sel:[0,0,1]
	v_permlane32_swap_b32_e32 v239, v235
	v_add_f32_e32 v239, v239, v235
	v_fma_f32 v2, v2, v217, v239
	v_mov_b32_e32 v217, 1.0
	s_waitcnt vmcnt(0) lgkmcnt(0)
	s_cmp_eq_u32 s48, 0
	s_cbranch_scc1 .Lm_bi11
	v_pk_mul_f32 v[226:227], v[226:227], s[50:51]
	v_pk_mul_f32 v[228:229], v[228:229], s[50:51]
	v_pk_mul_f32 v[230:231], v[230:231], s[50:51]
	v_pk_mul_f32 v[232:233], v[232:233], s[50:51]
	v_med3_f32 v226, v226, s33, v212
	v_med3_f32 v227, v227, s33, v212
	v_med3_f32 v228, v228, s33, v212
	v_med3_f32 v229, v229, s33, v212
	v_med3_f32 v230, v230, s33, v212
	v_med3_f32 v231, v231, s33, v212
	v_med3_f32 v232, v232, s33, v212
	v_med3_f32 v233, v233, s33, v212
	v_cvt_pk_fp8_f32 v244, v226, v227
	v_cvt_pk_fp8_f32 v245, v230, v231
	v_cvt_pk_fp8_f32 v244, v228, v229 op_sel:[0,0,1]
	v_cvt_pk_fp8_f32 v245, v232, v233 op_sel:[0,0,1]
	global_load_dword v226, v241, s[14:15]
	s_add_u32 s14, s14, s46
	s_addc_u32 s15, s15, 0
	global_load_dword v227, v241, s[14:15]
	s_add_u32 s14, s14, s46
	s_addc_u32 s15, s15, 0
	global_load_dword v228, v241, s[14:15]
	s_add_u32 s14, s14, s46
	s_addc_u32 s15, s15, 0
	global_load_dword v229, v241, s[14:15]
	s_add_u32 s14, s14, s46
	s_addc_u32 s15, s15, 0
	global_load_dword v230, v241, s[14:15]
	s_add_u32 s14, s14, s46
	s_addc_u32 s15, s15, 0
	global_load_dword v231, v241, s[14:15]
	s_add_u32 s14, s14, s46
	s_addc_u32 s15, s15, 0
	global_load_dword v232, v241, s[14:15]
	s_add_u32 s14, s14, s46
	s_addc_u32 s15, s15, 0
	global_load_dword v233, v241, s[14:15]
	s_add_u32 s14, s14, s46
	s_addc_u32 s15, s15, 0

.Lm_nm14:
	ds_read_b128 v[166:169], v207 offset:0
	ds_read_b128 v[170:173], v208 offset:0
	ds_read_b128 v[174:177], v207 offset:2048
	ds_read_b128 v[178:181], v208 offset:2048
	ds_read_b128 v[182:185], v207 offset:4096
	ds_read_b128 v[186:189], v208 offset:4096
	ds_read_b128 v[218:221], v207 offset:6144
	ds_read_b128 v[222:225], v208 offset:6144
	s_waitcnt lgkmcnt(6)
	v_mfma_f32_32x32x64_f8f6f4 v[52:67], v[248:255], v[166:173], v[52:67]
	ds_read_b128 v[166:169], v200 offset:40960
	ds_read_b128 v[170:173], v201 offset:40960
	v_max3_f32 v239, v124, v125, v126
	v_max3_f32 v235, v140, v141, v142
	v_max3_f32 v239, v239, v127, v128
	v_max3_f32 v235, v235, v143, v144
	v_max3_f32 v239, v239, v129, v130
	s_waitcnt lgkmcnt(6)
	v_mfma_f32_32x32x64_f8f6f4 v[36:51], v[248:255], v[174:181], v[36:51]
	ds_read_b128 v[174:177], v200 offset:45056
	ds_read_b128 v[178:181], v201 offset:45056
	v_max3_f32 v235, v235, v145, v146
	v_max3_f32 v239, v239, v131, v132
	v_max3_f32 v235, v235, v147, v148
	v_max3_f32 v239, v239, v133, v134
	v_max3_f32 v235, v235, v149, v150
	s_waitcnt lgkmcnt(6)
	v_mfma_f32_32x32x64_f8f6f4 v[20:35], v[248:255], v[182:189], v[20:35]
	ds_read_b128 v[182:185], v202 offset:40960
	ds_read_b128 v[186:189], v203 offset:40960
	v_max3_f32 v239, v239, v135, v136
	v_max3_f32 v235, v235, v151, v152
	v_max3_f32 v239, v239, v137, v138
	v_max3_f32 v235, v235, v153, v154
	s_waitcnt lgkmcnt(6)
	v_mfma_f32_32x32x64_f8f6f4 v[4:19], v[248:255], v[218:225], v[4:19]
	ds_read_b128 v[218:221], v202 offset:45056
	ds_read_b128 v[222:225], v203 offset:45056
	v_max3_f32 v239, v239, v139, v155
	v_max_f32_e32 v239, v239, v235
	v_mov_b32_e32 v234, v239
	s_waitcnt lgkmcnt(6)
	v_mfma_f32_32x32x64_f8f6f4 v[68:83], v[166:173], v[100:107], 0
	ds_read_b128 v[166:169], v242 offset:32768
	ds_read_b128 v[170:173], v243 offset:32768
	s_nop 1
	v_permlane32_swap_b32_e32 v239, v234
	v_max_f32_e32 v239, v239, v234
	v_sub_f32_e32 v235, v239, v216
	v_mul_f32_e32 v235, 0x3a93cd3a, v235
	v_cmp_ge_f32_e32 vcc, 2.0, v235
	s_cmp_eq_u64 vcc, exec
	s_cbranch_scc1 .Lm_nr15
	v_max_f32_e32 v235, v216, v239
	v_sub_f32_e32 v217, v216, v235
	v_mul_f32_e32 v217, 0x3ad53b94, v217
	v_exp_f32_e32 v217, v217
	v_mov_b32_e32 v216, v235
	s_and_saveexec_b64 s[6:7], s[0:1]
	ds_write_b32 v214, v217 offset:128
	s_or_b64 exec, exec, s[6:7]
	s_waitcnt lgkmcnt(0)
	ds_read_b128 v[84:87], v213 offset:128
	s_waitcnt lgkmcnt(0)
	v_pk_mul_f32 v[52:53], v[52:53], v[84:85]
	v_pk_mul_f32 v[54:55], v[54:55], v[86:87]
	v_pk_mul_f32 v[36:37], v[36:37], v[84:85]
	v_pk_mul_f32 v[38:39], v[38:39], v[86:87]
	v_pk_mul_f32 v[20:21], v[20:21], v[84:85]
	v_pk_mul_f32 v[22:23], v[22:23], v[86:87]
	v_pk_mul_f32 v[4:5], v[4:5], v[84:85]
	v_pk_mul_f32 v[6:7], v[6:7], v[86:87]
	ds_read_b128 v[84:87], v213 offset:160
	s_waitcnt lgkmcnt(0)
	v_pk_mul_f32 v[56:57], v[56:57], v[84:85]
	v_pk_mul_f32 v[58:59], v[58:59], v[86:87]
	v_pk_mul_f32 v[40:41], v[40:41], v[84:85]
	v_pk_mul_f32 v[42:43], v[42:43], v[86:87]
	v_pk_mul_f32 v[24:25], v[24:25], v[84:85]
	v_pk_mul_f32 v[26:27], v[26:27], v[86:87]
	v_pk_mul_f32 v[8:9], v[8:9], v[84:85]
	v_pk_mul_f32 v[10:11], v[10:11], v[86:87]
	ds_read_b128 v[84:87], v213 offset:192
	s_waitcnt lgkmcnt(0)
	v_pk_mul_f32 v[60:61], v[60:61], v[84:85]
	v_pk_mul_f32 v[62:63], v[62:63], v[86:87]
	v_pk_mul_f32 v[44:45], v[44:45], v[84:85]
	v_pk_mul_f32 v[46:47], v[46:47], v[86:87]
	v_pk_mul_f32 v[28:29], v[28:29], v[84:85]
	v_pk_mul_f32 v[30:31], v[30:31], v[86:87]
	v_pk_mul_f32 v[12:13], v[12:13], v[84:85]
	v_pk_mul_f32 v[14:15], v[14:15], v[86:87]
	ds_read_b128 v[84:87], v213 offset:224
	s_waitcnt lgkmcnt(0)
	v_pk_mul_f32 v[64:65], v[64:65], v[84:85]
	v_pk_mul_f32 v[66:67], v[66:67], v[86:87]
	v_pk_mul_f32 v[48:49], v[48:49], v[84:85]
	v_pk_mul_f32 v[50:51], v[50:51], v[86:87]
	v_pk_mul_f32 v[32:33], v[32:33], v[84:85]
	v_pk_mul_f32 v[34:35], v[34:35], v[86:87]
	v_pk_mul_f32 v[16:17], v[16:17], v[84:85]
	v_pk_mul_f32 v[18:19], v[18:19], v[86:87]
.Lm_nr15:
	v_fmamk_f32 v190, v216, 0xbad53b94, v210
	v_fma_f32 v124, v124, s96, v190
	v_fma_f32 v125, v125, s96, v190
	v_fma_f32 v140, v140, s96, v190
	v_fma_f32 v141, v141, s96, v190
	v_fma_f32 v126, v126, s96, v190
	v_fma_f32 v127, v127, s96, v190
	v_fma_f32 v142, v142, s96, v190
	v_fma_f32 v143, v143, s96, v190
	v_fma_f32 v128, v128, s96, v190
	v_fma_f32 v129, v129, s96, v190
	v_fma_f32 v144, v144, s96, v190
	v_fma_f32 v145, v145, s96, v190
	v_fma_f32 v130, v130, s96, v190
	v_fma_f32 v131, v131, s96, v190
	v_fma_f32 v146, v146, s96, v190
	v_fma_f32 v147, v147, s96, v190
	v_fma_f32 v132, v132, s96, v190
	s_waitcnt lgkmcnt(6)
	v_mfma_f32_32x32x64_f8f6f4 v[84:99], v[174:181], v[100:107], 0
	ds_read_b128 v[174:177], v242 offset:36864
	ds_read_b128 v[178:181], v243 offset:36864
	v_fma_f32 v133, v133, s96, v190
	v_fma_f32 v148, v148, s96, v190
	v_fma_f32 v149, v149, s96, v190
	v_fma_f32 v134, v134, s96, v190
	v_fma_f32 v135, v135, s96, v190
	v_fma_f32 v150, v150, s96, v190
	v_fma_f32 v151, v151, s96, v190
	v_fma_f32 v136, v136, s96, v190
	v_fma_f32 v137, v137, s96, v190
	v_fma_f32 v152, v152, s96, v190
	v_fma_f32 v153, v153, s96, v190
	v_fma_f32 v138, v138, s96, v190
	v_fma_f32 v139, v139, s96, v190
	v_fma_f32 v154, v154, s96, v190
	v_fma_f32 v155, v155, s96, v190
	v_exp_f32_e32 v124, v124
	v_exp_f32_e32 v125, v125
	v_exp_f32_e32 v126, v126
	s_waitcnt lgkmcnt(6)
	v_mfma_f32_32x32x64_f8f6f4 v[68:83], v[182:189], v[108:115], v[68:83]
	v_exp_f32_e32 v127, v127
	v_exp_f32_e32 v128, v128
	v_exp_f32_e32 v129, v129
	v_exp_f32_e32 v130, v130
	v_exp_f32_e32 v131, v131
	v_exp_f32_e32 v132, v132
	v_exp_f32_e32 v133, v133
	s_waitcnt lgkmcnt(4)
	v_mfma_f32_32x32x64_f8f6f4 v[84:99], v[218:225], v[108:115], v[84:99]
	v_exp_f32_e32 v134, v134
	v_exp_f32_e32 v135, v135
	v_exp_f32_e32 v136, v136
	v_exp_f32_e32 v137, v137
	v_exp_f32_e32 v138, v138
	v_exp_f32_e32 v139, v139
	v_exp_f32_e32 v140, v140
	v_exp_f32_e32 v141, v141
	s_waitcnt lgkmcnt(2)
	v_mfma_f32_32x32x64_f8f6f4 v[68:83], v[166:173], v[116:123], v[68:83]
	v_exp_f32_e32 v142, v142
	v_exp_f32_e32 v143, v143
	v_exp_f32_e32 v144, v144
	v_exp_f32_e32 v145, v145
	v_exp_f32_e32 v146, v146
	v_exp_f32_e32 v147, v147
	v_exp_f32_e32 v148, v148
	s_waitcnt lgkmcnt(0)
	v_mfma_f32_32x32x64_f8f6f4 v[84:99], v[174:181], v[116:123], v[84:99]
	v_exp_f32_e32 v149, v149
	v_exp_f32_e32 v150, v150
	v_exp_f32_e32 v151, v151
	v_exp_f32_e32 v152, v152
	v_exp_f32_e32 v153, v153
	v_exp_f32_e32 v154, v154
	v_exp_f32_e32 v155, v155
.Lm_m13_end:
	s_sub_i32 s5, s77, 1
	s_cmp_ge_u32 s5, s42
	s_cbranch_scc1 .Lm_t16_end
	v_add_f32_e32 v192, v124, v126
	v_add_f32_e32 v193, v125, v127
	v_add_f32_e32 v234, v140, v142
	v_add_f32_e32 v235, v141, v143
	v_add_f32_e32 v192, v128, v192
	v_add_f32_e32 v193, v129, v193
	v_cvt_pk_fp8_f32 v248, v124, v125
	v_add_f32_e32 v234, v144, v234
	v_add_f32_e32 v235, v145, v235
	v_cvt_pk_fp8_f32 v249, v128, v129
	v_add_f32_e32 v192, v130, v192
	v_add_f32_e32 v193, v131, v193
	v_cvt_pk_fp8_f32 v250, v132, v133
	v_add_f32_e32 v234, v146, v234
	v_add_f32_e32 v235, v147, v235
	v_cvt_pk_fp8_f32 v251, v136, v137
	v_add_f32_e32 v192, v132, v192
	v_add_f32_e32 v193, v133, v193
	v_cvt_pk_fp8_f32 v252, v140, v141
	v_add_f32_e32 v234, v148, v234
	v_add_f32_e32 v235, v149, v235
	v_cvt_pk_fp8_f32 v253, v144, v145
	v_add_f32_e32 v192, v134, v192
	v_add_f32_e32 v193, v135, v193
	v_cvt_pk_fp8_f32 v254, v148, v149
	v_add_f32_e32 v234, v150, v234
	v_add_f32_e32 v235, v151, v235
	v_cvt_pk_fp8_f32 v255, v152, v153
	v_add_f32_e32 v192, v136, v192
	v_add_f32_e32 v193, v137, v193
	v_add_f32_e32 v234, v152, v234
	v_add_f32_e32 v235, v153, v235
	v_add_f32_e32 v192, v138, v192
	v_add_f32_e32 v193, v139, v193
	v_add_f32_e32 v234, v154, v234
	v_add_f32_e32 v235, v155, v235
	v_add_f32_e32 v192, v192, v234
	v_add_f32_e32 v193, v193, v235
	v_cvt_pk_fp8_f32 v248, v126, v127 op_sel:[0,0,1]
	v_cvt_pk_fp8_f32 v249, v130, v131 op_sel:[0,0,1]
	v_cvt_pk_fp8_f32 v250, v134, v135 op_sel:[0,0,1]
	v_cvt_pk_fp8_f32 v251, v138, v139 op_sel:[0,0,1]
	v_add_f32_e32 v239, v192, v193
	v_cvt_pk_fp8_f32 v252, v142, v143 op_sel:[0,0,1]
	v_cvt_pk_fp8_f32 v253, v146, v147 op_sel:[0,0,1]
	v_mov_b32_e32 v235, v239
	v_cvt_pk_fp8_f32 v254, v150, v151 op_sel:[0,0,1]
	v_cvt_pk_fp8_f32 v255, v154, v155 op_sel:[0,0,1]
	v_permlane32_swap_b32_e32 v239, v235
	v_add_f32_e32 v239, v239, v235
	v_fma_f32 v2, v2, v217, v239
	v_mov_b32_e32 v217, 1.0

.Lm_nm22:
	ds_read_b128 v[166:169], v207 offset:16384
	ds_read_b128 v[170:173], v208 offset:16384
	ds_read_b128 v[174:177], v207 offset:18432
	ds_read_b128 v[178:181], v208 offset:18432
	ds_read_b128 v[182:185], v207 offset:20480
	ds_read_b128 v[186:189], v208 offset:20480
	ds_read_b128 v[218:221], v207 offset:22528
	ds_read_b128 v[222:225], v208 offset:22528
	s_waitcnt lgkmcnt(6)
	v_mfma_f32_32x32x64_f8f6f4 v[52:67], v[248:255], v[166:173], v[52:67]
	ds_read_b128 v[166:169], v200 offset:57344
	ds_read_b128 v[170:173], v201 offset:57344
	v_max3_f32 v239, v68, v69, v70
	v_max3_f32 v235, v84, v85, v86
	v_max3_f32 v239, v239, v71, v72
	v_max3_f32 v235, v235, v87, v88
	v_max3_f32 v239, v239, v73, v74
	s_waitcnt lgkmcnt(6)
	v_mfma_f32_32x32x64_f8f6f4 v[36:51], v[248:255], v[174:181], v[36:51]
	ds_read_b128 v[174:177], v200 offset:61440
	ds_read_b128 v[178:181], v201 offset:61440
	v_max3_f32 v235, v235, v89, v90
	v_max3_f32 v239, v239, v75, v76
	v_max3_f32 v235, v235, v91, v92
	v_max3_f32 v239, v239, v77, v78
	v_max3_f32 v235, v235, v93, v94
	s_waitcnt lgkmcnt(6)
	v_mfma_f32_32x32x64_f8f6f4 v[20:35], v[248:255], v[182:189], v[20:35]
	ds_read_b128 v[182:185], v202 offset:57344
	ds_read_b128 v[186:189], v203 offset:57344
	v_max3_f32 v239, v239, v79, v80
	v_max3_f32 v235, v235, v95, v96
	v_max3_f32 v239, v239, v81, v82
	v_max3_f32 v235, v235, v97, v98
	s_waitcnt lgkmcnt(6)
	v_mfma_f32_32x32x64_f8f6f4 v[4:19], v[248:255], v[218:225], v[4:19]
	ds_read_b128 v[218:221], v202 offset:61440
	ds_read_b128 v[222:225], v203 offset:61440
	v_max3_f32 v239, v239, v83, v99
	v_max_f32_e32 v239, v239, v235
	v_mov_b32_e32 v234, v239
	s_waitcnt lgkmcnt(6)
	v_mfma_f32_32x32x64_f8f6f4 v[124:139], v[166:173], v[100:107], 0
	ds_read_b128 v[166:169], v242 offset:40960
	ds_read_b128 v[170:173], v243 offset:40960
	s_nop 1
	v_permlane32_swap_b32_e32 v239, v234
	v_max_f32_e32 v239, v239, v234
	v_sub_f32_e32 v235, v239, v216
	v_mul_f32_e32 v235, 0x3a93cd3a, v235
	v_cmp_ge_f32_e32 vcc, 2.0, v235
	s_cmp_eq_u64 vcc, exec
	s_cbranch_scc1 .Lm_nr23
	v_max_f32_e32 v235, v216, v239
	v_sub_f32_e32 v217, v216, v235
	v_mul_f32_e32 v217, 0x3ad53b94, v217
	v_exp_f32_e32 v217, v217
	v_mov_b32_e32 v216, v235
	s_and_saveexec_b64 s[6:7], s[0:1]
	ds_write_b32 v214, v217 offset:128
	s_or_b64 exec, exec, s[6:7]
	s_waitcnt lgkmcnt(0)
	ds_read_b128 v[140:143], v213 offset:128
	s_waitcnt lgkmcnt(0)
	v_pk_mul_f32 v[52:53], v[52:53], v[140:141]
	v_pk_mul_f32 v[54:55], v[54:55], v[142:143]
	v_pk_mul_f32 v[36:37], v[36:37], v[140:141]
	v_pk_mul_f32 v[38:39], v[38:39], v[142:143]
	v_pk_mul_f32 v[20:21], v[20:21], v[140:141]
	v_pk_mul_f32 v[22:23], v[22:23], v[142:143]
	v_pk_mul_f32 v[4:5], v[4:5], v[140:141]
	v_pk_mul_f32 v[6:7], v[6:7], v[142:143]
	ds_read_b128 v[140:143], v213 offset:160
	s_waitcnt lgkmcnt(0)
	v_pk_mul_f32 v[56:57], v[56:57], v[140:141]
	v_pk_mul_f32 v[58:59], v[58:59], v[142:143]
	v_pk_mul_f32 v[40:41], v[40:41], v[140:141]
	v_pk_mul_f32 v[42:43], v[42:43], v[142:143]
	v_pk_mul_f32 v[24:25], v[24:25], v[140:141]
	v_pk_mul_f32 v[26:27], v[26:27], v[142:143]
	v_pk_mul_f32 v[8:9], v[8:9], v[140:141]
	v_pk_mul_f32 v[10:11], v[10:11], v[142:143]
	ds_read_b128 v[140:143], v213 offset:192
	s_waitcnt lgkmcnt(0)
	v_pk_mul_f32 v[60:61], v[60:61], v[140:141]
	v_pk_mul_f32 v[62:63], v[62:63], v[142:143]
	v_pk_mul_f32 v[44:45], v[44:45], v[140:141]
	v_pk_mul_f32 v[46:47], v[46:47], v[142:143]
	v_pk_mul_f32 v[28:29], v[28:29], v[140:141]
	v_pk_mul_f32 v[30:31], v[30:31], v[142:143]
	v_pk_mul_f32 v[12:13], v[12:13], v[140:141]
	v_pk_mul_f32 v[14:15], v[14:15], v[142:143]
	ds_read_b128 v[140:143], v213 offset:224
	s_waitcnt lgkmcnt(0)
	v_pk_mul_f32 v[64:65], v[64:65], v[140:141]
	v_pk_mul_f32 v[66:67], v[66:67], v[142:143]
	v_pk_mul_f32 v[48:49], v[48:49], v[140:141]
	v_pk_mul_f32 v[50:51], v[50:51], v[142:143]
	v_pk_mul_f32 v[32:33], v[32:33], v[140:141]
	v_pk_mul_f32 v[34:35], v[34:35], v[142:143]
	v_pk_mul_f32 v[16:17], v[16:17], v[140:141]
	v_pk_mul_f32 v[18:19], v[18:19], v[142:143]
.Lm_nr23:
	v_fmamk_f32 v190, v216, 0xbad53b94, v210
	v_fma_f32 v68, v68, s96, v190
	v_fma_f32 v69, v69, s96, v190
	v_fma_f32 v84, v84, s96, v190
	v_fma_f32 v85, v85, s96, v190
	v_fma_f32 v70, v70, s96, v190
	v_fma_f32 v71, v71, s96, v190
	v_fma_f32 v86, v86, s96, v190
	v_fma_f32 v87, v87, s96, v190
	v_fma_f32 v72, v72, s96, v190
	v_fma_f32 v73, v73, s96, v190
	v_fma_f32 v88, v88, s96, v190
	v_fma_f32 v89, v89, s96, v190
	v_fma_f32 v74, v74, s96, v190
	v_fma_f32 v75, v75, s96, v190
	v_fma_f32 v90, v90, s96, v190
	v_fma_f32 v91, v91, s96, v190
	v_fma_f32 v76, v76, s96, v190
	s_waitcnt lgkmcnt(6)
	v_mfma_f32_32x32x64_f8f6f4 v[140:155], v[174:181], v[100:107], 0
	ds_read_b128 v[174:177], v242 offset:45056
	ds_read_b128 v[178:181], v243 offset:45056
	v_fma_f32 v77, v77, s96, v190
	v_fma_f32 v92, v92, s96, v190
	v_fma_f32 v93, v93, s96, v190
	v_fma_f32 v78, v78, s96, v190
	v_fma_f32 v79, v79, s96, v190
	v_fma_f32 v94, v94, s96, v190
	v_fma_f32 v95, v95, s96, v190
	v_fma_f32 v80, v80, s96, v190
	v_fma_f32 v81, v81, s96, v190
	v_fma_f32 v96, v96, s96, v190
	v_fma_f32 v97, v97, s96, v190
	v_fma_f32 v82, v82, s96, v190
	v_fma_f32 v83, v83, s96, v190
	v_fma_f32 v98, v98, s96, v190
	v_fma_f32 v99, v99, s96, v190
	v_exp_f32_e32 v68, v68
	v_exp_f32_e32 v69, v69
	v_exp_f32_e32 v70, v70
	s_waitcnt lgkmcnt(6)
	v_mfma_f32_32x32x64_f8f6f4 v[124:139], v[182:189], v[108:115], v[124:139]
	v_exp_f32_e32 v71, v71
	v_exp_f32_e32 v72, v72
	v_exp_f32_e32 v73, v73
	v_exp_f32_e32 v74, v74
	v_exp_f32_e32 v75, v75
	v_exp_f32_e32 v76, v76
	v_exp_f32_e32 v77, v77
	s_waitcnt lgkmcnt(4)
	v_mfma_f32_32x32x64_f8f6f4 v[140:155], v[218:225], v[108:115], v[140:155]
	v_exp_f32_e32 v78, v78
	v_exp_f32_e32 v79, v79
	v_exp_f32_e32 v80, v80
	v_exp_f32_e32 v81, v81
	v_exp_f32_e32 v82, v82
	v_exp_f32_e32 v83, v83
	v_exp_f32_e32 v84, v84
	v_exp_f32_e32 v85, v85
	s_waitcnt lgkmcnt(2)
	v_mfma_f32_32x32x64_f8f6f4 v[124:139], v[166:173], v[116:123], v[124:139]
	v_exp_f32_e32 v86, v86
	v_exp_f32_e32 v87, v87
	v_exp_f32_e32 v88, v88
	v_exp_f32_e32 v89, v89
	v_exp_f32_e32 v90, v90
	v_exp_f32_e32 v91, v91
	v_exp_f32_e32 v92, v92
	s_waitcnt lgkmcnt(0)
	v_mfma_f32_32x32x64_f8f6f4 v[140:155], v[174:181], v[116:123], v[140:155]
	v_exp_f32_e32 v93, v93
	v_exp_f32_e32 v94, v94
	v_exp_f32_e32 v95, v95
	v_exp_f32_e32 v96, v96
	v_exp_f32_e32 v97, v97
	v_exp_f32_e32 v98, v98
	v_exp_f32_e32 v99, v99
.Lm_m21_end:
	s_sub_i32 s5, s77, 1
	s_cmp_ge_u32 s5, s42
	s_cbranch_scc1 .Lm_t24_end
	v_add_f32_e32 v192, v68, v70
	v_add_f32_e32 v193, v69, v71
	v_add_f32_e32 v234, v84, v86
	v_add_f32_e32 v235, v85, v87
	v_add_f32_e32 v192, v72, v192
	v_add_f32_e32 v193, v73, v193
	v_cvt_pk_fp8_f32 v248, v68, v69
	v_add_f32_e32 v234, v88, v234
	v_add_f32_e32 v235, v89, v235
	v_cvt_pk_fp8_f32 v249, v72, v73
	v_add_f32_e32 v192, v74, v192
	v_add_f32_e32 v193, v75, v193
	v_cvt_pk_fp8_f32 v250, v76, v77
	v_add_f32_e32 v234, v90, v234
	v_add_f32_e32 v235, v91, v235
	v_cvt_pk_fp8_f32 v251, v80, v81
	v_add_f32_e32 v192, v76, v192
	v_add_f32_e32 v193, v77, v193
	v_cvt_pk_fp8_f32 v252, v84, v85
	v_add_f32_e32 v234, v92, v234
	v_add_f32_e32 v235, v93, v235
	v_cvt_pk_fp8_f32 v253, v88, v89
	v_add_f32_e32 v192, v78, v192
	v_add_f32_e32 v193, v79, v193
	v_cvt_pk_fp8_f32 v254, v92, v93
	v_add_f32_e32 v234, v94, v234
	v_add_f32_e32 v235, v95, v235
	v_cvt_pk_fp8_f32 v255, v96, v97
	v_add_f32_e32 v192, v80, v192
	v_add_f32_e32 v193, v81, v193
	v_add_f32_e32 v234, v96, v234
	v_add_f32_e32 v235, v97, v235
	v_add_f32_e32 v192, v82, v192
	v_add_f32_e32 v193, v83, v193
	v_add_f32_e32 v234, v98, v234
	v_add_f32_e32 v235, v99, v235
	v_add_f32_e32 v192, v192, v234
	v_add_f32_e32 v193, v193, v235
	v_cvt_pk_fp8_f32 v248, v70, v71 op_sel:[0,0,1]
	v_cvt_pk_fp8_f32 v249, v74, v75 op_sel:[0,0,1]
	v_cvt_pk_fp8_f32 v250, v78, v79 op_sel:[0,0,1]
	v_cvt_pk_fp8_f32 v251, v82, v83 op_sel:[0,0,1]
	v_add_f32_e32 v239, v192, v193
	v_cvt_pk_fp8_f32 v252, v86, v87 op_sel:[0,0,1]
	v_cvt_pk_fp8_f32 v253, v90, v91 op_sel:[0,0,1]
	v_mov_b32_e32 v235, v239
	v_cvt_pk_fp8_f32 v254, v94, v95 op_sel:[0,0,1]
	v_cvt_pk_fp8_f32 v255, v98, v99 op_sel:[0,0,1]
	v_permlane32_swap_b32_e32 v239, v235
	v_add_f32_e32 v239, v239, v235
	v_fma_f32 v2, v2, v217, v239
	v_mov_b32_e32 v217, 1.0

.Lm_nm28:
	ds_read_b128 v[166:169], v207 offset:8192
	ds_read_b128 v[170:173], v208 offset:8192
	ds_read_b128 v[174:177], v207 offset:10240
	ds_read_b128 v[178:181], v208 offset:10240
	ds_read_b128 v[182:185], v207 offset:12288
	ds_read_b128 v[186:189], v208 offset:12288
	ds_read_b128 v[218:221], v207 offset:14336
	ds_read_b128 v[222:225], v208 offset:14336
	s_waitcnt lgkmcnt(6)
	v_mfma_f32_32x32x64_f8f6f4 v[52:67], v[248:255], v[166:173], v[52:67]
	ds_read_b128 v[166:169], v200 offset:32768
	ds_read_b128 v[170:173], v201 offset:32768
	v_max3_f32 v239, v124, v125, v126
	v_max3_f32 v235, v140, v141, v142
	v_max3_f32 v239, v239, v127, v128
	v_max3_f32 v235, v235, v143, v144
	v_max3_f32 v239, v239, v129, v130
	s_waitcnt lgkmcnt(6)
	v_mfma_f32_32x32x64_f8f6f4 v[36:51], v[248:255], v[174:181], v[36:51]
	ds_read_b128 v[174:177], v200 offset:36864
	ds_read_b128 v[178:181], v201 offset:36864
	v_max3_f32 v235, v235, v145, v146
	v_max3_f32 v239, v239, v131, v132
	v_max3_f32 v235, v235, v147, v148
	v_max3_f32 v239, v239, v133, v134
	v_max3_f32 v235, v235, v149, v150
	s_waitcnt lgkmcnt(6)
	v_mfma_f32_32x32x64_f8f6f4 v[20:35], v[248:255], v[182:189], v[20:35]
	ds_read_b128 v[182:185], v202 offset:32768
	ds_read_b128 v[186:189], v203 offset:32768
	v_max3_f32 v239, v239, v135, v136
	v_max3_f32 v235, v235, v151, v152
	v_max3_f32 v239, v239, v137, v138
	v_max3_f32 v235, v235, v153, v154
	s_waitcnt lgkmcnt(6)
	v_mfma_f32_32x32x64_f8f6f4 v[4:19], v[248:255], v[218:225], v[4:19]
	ds_read_b128 v[218:221], v202 offset:36864
	ds_read_b128 v[222:225], v203 offset:36864
	v_max3_f32 v239, v239, v139, v155
	v_max_f32_e32 v239, v239, v235
	v_mov_b32_e32 v234, v239
	s_waitcnt lgkmcnt(6)
	v_mfma_f32_32x32x64_f8f6f4 v[68:83], v[166:173], v[100:107], 0
	ds_read_b128 v[166:169], v242 offset:0
	ds_read_b128 v[170:173], v243 offset:0
	s_nop 1
	v_permlane32_swap_b32_e32 v239, v234
	v_max_f32_e32 v239, v239, v234
	v_sub_f32_e32 v235, v239, v216
	v_mul_f32_e32 v235, 0x3a93cd3a, v235
	v_cmp_ge_f32_e32 vcc, 2.0, v235
	s_cmp_eq_u64 vcc, exec
	s_cbranch_scc1 .Lm_nr29
	v_max_f32_e32 v235, v216, v239
	v_sub_f32_e32 v217, v216, v235
	v_mul_f32_e32 v217, 0x3ad53b94, v217
	v_exp_f32_e32 v217, v217
	v_mov_b32_e32 v216, v235
	s_and_saveexec_b64 s[6:7], s[0:1]
	ds_write_b32 v214, v217 offset:128
	s_or_b64 exec, exec, s[6:7]
	s_waitcnt lgkmcnt(0)
	ds_read_b128 v[84:87], v213 offset:128
	s_waitcnt lgkmcnt(0)
	v_pk_mul_f32 v[52:53], v[52:53], v[84:85]
	v_pk_mul_f32 v[54:55], v[54:55], v[86:87]
	v_pk_mul_f32 v[36:37], v[36:37], v[84:85]
	v_pk_mul_f32 v[38:39], v[38:39], v[86:87]
	v_pk_mul_f32 v[20:21], v[20:21], v[84:85]
	v_pk_mul_f32 v[22:23], v[22:23], v[86:87]
	v_pk_mul_f32 v[4:5], v[4:5], v[84:85]
	v_pk_mul_f32 v[6:7], v[6:7], v[86:87]
	ds_read_b128 v[84:87], v213 offset:160
	s_waitcnt lgkmcnt(0)
	v_pk_mul_f32 v[56:57], v[56:57], v[84:85]
	v_pk_mul_f32 v[58:59], v[58:59], v[86:87]
	v_pk_mul_f32 v[40:41], v[40:41], v[84:85]
	v_pk_mul_f32 v[42:43], v[42:43], v[86:87]
	v_pk_mul_f32 v[24:25], v[24:25], v[84:85]
	v_pk_mul_f32 v[26:27], v[26:27], v[86:87]
	v_pk_mul_f32 v[8:9], v[8:9], v[84:85]
	v_pk_mul_f32 v[10:11], v[10:11], v[86:87]
	ds_read_b128 v[84:87], v213 offset:192
	s_waitcnt lgkmcnt(0)
	v_pk_mul_f32 v[60:61], v[60:61], v[84:85]
	v_pk_mul_f32 v[62:63], v[62:63], v[86:87]
	v_pk_mul_f32 v[44:45], v[44:45], v[84:85]
	v_pk_mul_f32 v[46:47], v[46:47], v[86:87]
	v_pk_mul_f32 v[28:29], v[28:29], v[84:85]
	v_pk_mul_f32 v[30:31], v[30:31], v[86:87]
	v_pk_mul_f32 v[12:13], v[12:13], v[84:85]
	v_pk_mul_f32 v[14:15], v[14:15], v[86:87]
	ds_read_b128 v[84:87], v213 offset:224
	s_waitcnt lgkmcnt(0)
	v_pk_mul_f32 v[64:65], v[64:65], v[84:85]
	v_pk_mul_f32 v[66:67], v[66:67], v[86:87]
	v_pk_mul_f32 v[48:49], v[48:49], v[84:85]
	v_pk_mul_f32 v[50:51], v[50:51], v[86:87]
	v_pk_mul_f32 v[32:33], v[32:33], v[84:85]
	v_pk_mul_f32 v[34:35], v[34:35], v[86:87]
	v_pk_mul_f32 v[16:17], v[16:17], v[84:85]
	v_pk_mul_f32 v[18:19], v[18:19], v[86:87]
.Lm_nr29:
	v_fmamk_f32 v190, v216, 0xbad53b94, v210
	v_fma_f32 v124, v124, s96, v190
	v_fma_f32 v125, v125, s96, v190
	v_fma_f32 v140, v140, s96, v190
	v_fma_f32 v141, v141, s96, v190
	v_fma_f32 v126, v126, s96, v190
	v_fma_f32 v127, v127, s96, v190
	v_fma_f32 v142, v142, s96, v190
	v_fma_f32 v143, v143, s96, v190
	v_fma_f32 v128, v128, s96, v190
	v_fma_f32 v129, v129, s96, v190
	v_fma_f32 v144, v144, s96, v190
	v_fma_f32 v145, v145, s96, v190
	v_fma_f32 v130, v130, s96, v190
	v_fma_f32 v131, v131, s96, v190
	v_fma_f32 v146, v146, s96, v190
	v_fma_f32 v147, v147, s96, v190
	v_fma_f32 v132, v132, s96, v190
	s_waitcnt lgkmcnt(6)
	v_mfma_f32_32x32x64_f8f6f4 v[84:99], v[174:181], v[100:107], 0
	ds_read_b128 v[174:177], v242 offset:4096
	ds_read_b128 v[178:181], v243 offset:4096
	v_fma_f32 v133, v133, s96, v190
	v_fma_f32 v148, v148, s96, v190
	v_fma_f32 v149, v149, s96, v190
	v_fma_f32 v134, v134, s96, v190
	v_fma_f32 v135, v135, s96, v190
	v_fma_f32 v150, v150, s96, v190
	v_fma_f32 v151, v151, s96, v190
	v_fma_f32 v136, v136, s96, v190
	v_fma_f32 v137, v137, s96, v190
	v_fma_f32 v152, v152, s96, v190
	v_fma_f32 v153, v153, s96, v190
	v_fma_f32 v138, v138, s96, v190
	v_fma_f32 v139, v139, s96, v190
	v_fma_f32 v154, v154, s96, v190
	v_fma_f32 v155, v155, s96, v190
	v_exp_f32_e32 v124, v124
	v_exp_f32_e32 v125, v125
	v_exp_f32_e32 v126, v126
	s_waitcnt lgkmcnt(6)
	v_mfma_f32_32x32x64_f8f6f4 v[68:83], v[182:189], v[108:115], v[68:83]
	v_exp_f32_e32 v127, v127
	v_exp_f32_e32 v128, v128
	v_exp_f32_e32 v129, v129
	v_exp_f32_e32 v130, v130
	v_exp_f32_e32 v131, v131
	v_exp_f32_e32 v132, v132
	v_exp_f32_e32 v133, v133
	s_waitcnt lgkmcnt(4)
	v_mfma_f32_32x32x64_f8f6f4 v[84:99], v[218:225], v[108:115], v[84:99]
	v_exp_f32_e32 v134, v134
	v_exp_f32_e32 v135, v135
	v_exp_f32_e32 v136, v136
	v_exp_f32_e32 v137, v137
	v_exp_f32_e32 v138, v138
	v_exp_f32_e32 v139, v139
	v_exp_f32_e32 v140, v140
	v_exp_f32_e32 v141, v141
	s_waitcnt lgkmcnt(2)
	v_mfma_f32_32x32x64_f8f6f4 v[68:83], v[166:173], v[116:123], v[68:83]
	v_exp_f32_e32 v142, v142
	v_exp_f32_e32 v143, v143
	v_exp_f32_e32 v144, v144
	v_exp_f32_e32 v145, v145
	v_exp_f32_e32 v146, v146
	v_exp_f32_e32 v147, v147
	v_exp_f32_e32 v148, v148
	s_waitcnt lgkmcnt(0)
	v_mfma_f32_32x32x64_f8f6f4 v[84:99], v[174:181], v[116:123], v[84:99]
	v_exp_f32_e32 v149, v149
	v_exp_f32_e32 v150, v150
	v_exp_f32_e32 v151, v151
	v_exp_f32_e32 v152, v152
	v_exp_f32_e32 v153, v153
	v_exp_f32_e32 v154, v154
	v_exp_f32_e32 v155, v155

.Lm_nm36:
	ds_read_b128 v[166:169], v207 offset:24576
	ds_read_b128 v[170:173], v208 offset:24576
	ds_read_b128 v[174:177], v207 offset:26624
	ds_read_b128 v[178:181], v208 offset:26624
	ds_read_b128 v[182:185], v207 offset:28672
	ds_read_b128 v[186:189], v208 offset:28672
	ds_read_b128 v[218:221], v207 offset:30720
	ds_read_b128 v[222:225], v208 offset:30720
	s_waitcnt lgkmcnt(6)
	v_mfma_f32_32x32x64_f8f6f4 v[52:67], v[248:255], v[166:173], v[52:67]
	ds_read_b128 v[166:169], v200 offset:49152
	ds_read_b128 v[170:173], v201 offset:49152
	v_max3_f32 v239, v68, v69, v70
	v_max3_f32 v235, v84, v85, v86
	v_max3_f32 v239, v239, v71, v72
	v_max3_f32 v235, v235, v87, v88
	v_max3_f32 v239, v239, v73, v74
	s_waitcnt lgkmcnt(6)
	v_mfma_f32_32x32x64_f8f6f4 v[36:51], v[248:255], v[174:181], v[36:51]
	ds_read_b128 v[174:177], v200 offset:53248
	ds_read_b128 v[178:181], v201 offset:53248
	v_max3_f32 v235, v235, v89, v90
	v_max3_f32 v239, v239, v75, v76
	v_max3_f32 v235, v235, v91, v92
	v_max3_f32 v239, v239, v77, v78
	v_max3_f32 v235, v235, v93, v94
	s_waitcnt lgkmcnt(6)
	v_mfma_f32_32x32x64_f8f6f4 v[20:35], v[248:255], v[182:189], v[20:35]
	ds_read_b128 v[182:185], v202 offset:49152
	ds_read_b128 v[186:189], v203 offset:49152
	v_max3_f32 v239, v239, v79, v80
	v_max3_f32 v235, v235, v95, v96
	v_max3_f32 v239, v239, v81, v82
	v_max3_f32 v235, v235, v97, v98
	s_waitcnt lgkmcnt(6)
	v_mfma_f32_32x32x64_f8f6f4 v[4:19], v[248:255], v[218:225], v[4:19]
	ds_read_b128 v[218:221], v202 offset:53248
	ds_read_b128 v[222:225], v203 offset:53248
	v_max3_f32 v239, v239, v83, v99
	v_max_f32_e32 v239, v239, v235
	v_mov_b32_e32 v234, v239
	s_waitcnt lgkmcnt(6)
	v_mfma_f32_32x32x64_f8f6f4 v[124:139], v[166:173], v[100:107], 0
	ds_read_b128 v[166:169], v242 offset:8192
	ds_read_b128 v[170:173], v243 offset:8192
	s_nop 1
	v_permlane32_swap_b32_e32 v239, v234
	v_max_f32_e32 v239, v239, v234
	v_sub_f32_e32 v235, v239, v216
	v_mul_f32_e32 v235, 0x3a93cd3a, v235
	v_cmp_ge_f32_e32 vcc, 2.0, v235
	s_cmp_eq_u64 vcc, exec
	s_cbranch_scc1 .Lm_nr37
	v_max_f32_e32 v235, v216, v239
	v_sub_f32_e32 v217, v216, v235
	v_mul_f32_e32 v217, 0x3ad53b94, v217
	v_exp_f32_e32 v217, v217
	v_mov_b32_e32 v216, v235
	s_and_saveexec_b64 s[6:7], s[0:1]
	ds_write_b32 v214, v217 offset:128
	s_or_b64 exec, exec, s[6:7]
	s_waitcnt lgkmcnt(0)
	ds_read_b128 v[140:143], v213 offset:128
	s_waitcnt lgkmcnt(0)
	v_pk_mul_f32 v[52:53], v[52:53], v[140:141]
	v_pk_mul_f32 v[54:55], v[54:55], v[142:143]
	v_pk_mul_f32 v[36:37], v[36:37], v[140:141]
	v_pk_mul_f32 v[38:39], v[38:39], v[142:143]
	v_pk_mul_f32 v[20:21], v[20:21], v[140:141]
	v_pk_mul_f32 v[22:23], v[22:23], v[142:143]
	v_pk_mul_f32 v[4:5], v[4:5], v[140:141]
	v_pk_mul_f32 v[6:7], v[6:7], v[142:143]
	ds_read_b128 v[140:143], v213 offset:160
	s_waitcnt lgkmcnt(0)
	v_pk_mul_f32 v[56:57], v[56:57], v[140:141]
	v_pk_mul_f32 v[58:59], v[58:59], v[142:143]
	v_pk_mul_f32 v[40:41], v[40:41], v[140:141]
	v_pk_mul_f32 v[42:43], v[42:43], v[142:143]
	v_pk_mul_f32 v[24:25], v[24:25], v[140:141]
	v_pk_mul_f32 v[26:27], v[26:27], v[142:143]
	v_pk_mul_f32 v[8:9], v[8:9], v[140:141]
	v_pk_mul_f32 v[10:11], v[10:11], v[142:143]
	ds_read_b128 v[140:143], v213 offset:192
	s_waitcnt lgkmcnt(0)
	v_pk_mul_f32 v[60:61], v[60:61], v[140:141]
	v_pk_mul_f32 v[62:63], v[62:63], v[142:143]
	v_pk_mul_f32 v[44:45], v[44:45], v[140:141]
	v_pk_mul_f32 v[46:47], v[46:47], v[142:143]
	v_pk_mul_f32 v[28:29], v[28:29], v[140:141]
	v_pk_mul_f32 v[30:31], v[30:31], v[142:143]
	v_pk_mul_f32 v[12:13], v[12:13], v[140:141]
	v_pk_mul_f32 v[14:15], v[14:15], v[142:143]
	ds_read_b128 v[140:143], v213 offset:224
	s_waitcnt lgkmcnt(0)
	v_pk_mul_f32 v[64:65], v[64:65], v[140:141]
	v_pk_mul_f32 v[66:67], v[66:67], v[142:143]
	v_pk_mul_f32 v[48:49], v[48:49], v[140:141]
	v_pk_mul_f32 v[50:51], v[50:51], v[142:143]
	v_pk_mul_f32 v[32:33], v[32:33], v[140:141]
	v_pk_mul_f32 v[34:35], v[34:35], v[142:143]
	v_pk_mul_f32 v[16:17], v[16:17], v[140:141]
	v_pk_mul_f32 v[18:19], v[18:19], v[142:143]
.Lm_nr37:
	v_fmamk_f32 v190, v216, 0xbad53b94, v210
	v_fma_f32 v68, v68, s96, v190
	v_fma_f32 v69, v69, s96, v190
	v_fma_f32 v84, v84, s96, v190
	v_fma_f32 v85, v85, s96, v190
	v_fma_f32 v70, v70, s96, v190
	v_fma_f32 v71, v71, s96, v190
	v_fma_f32 v86, v86, s96, v190
	v_fma_f32 v87, v87, s96, v190
	v_fma_f32 v72, v72, s96, v190
	v_fma_f32 v73, v73, s96, v190
	v_fma_f32 v88, v88, s96, v190
	v_fma_f32 v89, v89, s96, v190
	v_fma_f32 v74, v74, s96, v190
	v_fma_f32 v75, v75, s96, v190
	v_fma_f32 v90, v90, s96, v190
	v_fma_f32 v91, v91, s96, v190
	v_fma_f32 v76, v76, s96, v190
	s_waitcnt lgkmcnt(6)
	v_mfma_f32_32x32x64_f8f6f4 v[140:155], v[174:181], v[100:107], 0
	ds_read_b128 v[174:177], v242 offset:12288
	ds_read_b128 v[178:181], v243 offset:12288
	v_fma_f32 v77, v77, s96, v190
	v_fma_f32 v92, v92, s96, v190
	v_fma_f32 v93, v93, s96, v190
	v_fma_f32 v78, v78, s96, v190
	v_fma_f32 v79, v79, s96, v190
	v_fma_f32 v94, v94, s96, v190
	v_fma_f32 v95, v95, s96, v190
	v_fma_f32 v80, v80, s96, v190
	v_fma_f32 v81, v81, s96, v190
	v_fma_f32 v96, v96, s96, v190
	v_fma_f32 v97, v97, s96, v190
	v_fma_f32 v82, v82, s96, v190
	v_fma_f32 v83, v83, s96, v190
	v_fma_f32 v98, v98, s96, v190
	v_fma_f32 v99, v99, s96, v190
	v_exp_f32_e32 v68, v68
	v_exp_f32_e32 v69, v69
	v_exp_f32_e32 v70, v70
	s_waitcnt lgkmcnt(6)
	v_mfma_f32_32x32x64_f8f6f4 v[124:139], v[182:189], v[108:115], v[124:139]
	v_exp_f32_e32 v71, v71
	v_exp_f32_e32 v72, v72
	v_exp_f32_e32 v73, v73
	v_exp_f32_e32 v74, v74
	v_exp_f32_e32 v75, v75
	v_exp_f32_e32 v76, v76
	v_exp_f32_e32 v77, v77
	s_waitcnt lgkmcnt(4)
	v_mfma_f32_32x32x64_f8f6f4 v[140:155], v[218:225], v[108:115], v[140:155]
	v_exp_f32_e32 v78, v78
	v_exp_f32_e32 v79, v79
	v_exp_f32_e32 v80, v80
	v_exp_f32_e32 v81, v81
	v_exp_f32_e32 v82, v82
	v_exp_f32_e32 v83, v83
	v_exp_f32_e32 v84, v84
	v_exp_f32_e32 v85, v85
	s_waitcnt lgkmcnt(2)
	v_mfma_f32_32x32x64_f8f6f4 v[124:139], v[166:173], v[116:123], v[124:139]
	v_exp_f32_e32 v86, v86
	v_exp_f32_e32 v87, v87
	v_exp_f32_e32 v88, v88
	v_exp_f32_e32 v89, v89
	v_exp_f32_e32 v90, v90
	v_exp_f32_e32 v91, v91
	v_exp_f32_e32 v92, v92
	s_waitcnt lgkmcnt(0)
	v_mfma_f32_32x32x64_f8f6f4 v[140:155], v[174:181], v[116:123], v[140:155]
	v_exp_f32_e32 v93, v93
	v_exp_f32_e32 v94, v94
	v_exp_f32_e32 v95, v95
	v_exp_f32_e32 v96, v96
	v_exp_f32_e32 v97, v97
	v_exp_f32_e32 v98, v98
	v_exp_f32_e32 v99, v99

.Lm_t38_end:
	s_waitcnt vmcnt(0) lgkmcnt(0)
	s_cmp_eq_u32 s48, 0
	s_cbranch_scc1 .Lm_bi39
	v_pk_mul_f32 v[226:227], v[226:227], s[50:51]
	v_pk_mul_f32 v[228:229], v[228:229], s[50:51]
	v_pk_mul_f32 v[230:231], v[230:231], s[50:51]
	v_pk_mul_f32 v[232:233], v[232:233], s[50:51]
	v_med3_f32 v226, v226, s33, v212
	v_med3_f32 v227, v227, s33, v212
	v_med3_f32 v228, v228, s33, v212
	v_med3_f32 v229, v229, s33, v212
	v_med3_f32 v230, v230, s33, v212
	v_med3_f32 v231, v231, s33, v212
	v_med3_f32 v232, v232, s33, v212
	v_med3_f32 v233, v233, s33, v212
	v_cvt_pk_fp8_f32 v244, v226, v227
	v_cvt_pk_fp8_f32 v245, v230, v231
	v_cvt_pk_fp8_f32 v244, v228, v229 op_sel:[0,0,1]
	v_cvt_pk_fp8_f32 v245, v232, v233 op_sel:[0,0,1]
	global_load_dword v226, v241, s[14:15]
	s_add_u32 s14, s14, s46
	s_addc_u32 s15, s15, 0
	global_load_dword v227, v241, s[14:15]
	s_add_u32 s14, s14, s46
	s_addc_u32 s15, s15, 0
	global_load_dword v228, v241, s[14:15]
	s_add_u32 s14, s14, s46
	s_addc_u32 s15, s15, 0
	global_load_dword v229, v241, s[14:15]
	s_add_u32 s14, s14, s46
	s_addc_u32 s15, s15, 0
	global_load_dword v230, v241, s[14:15]
	s_add_u32 s14, s14, s46
	s_addc_u32 s15, s15, 0
	global_load_dword v231, v241, s[14:15]
	s_add_u32 s14, s14, s46
	s_addc_u32 s15, s15, 0
	global_load_dword v232, v241, s[14:15]
	s_add_u32 s14, s14, s46
	s_addc_u32 s15, s15, 0
	global_load_dword v233, v241, s[14:15]
	s_add_u32 s14, s14, s46
	s_addc_u32 s15, s15, 0
.Lm_bi39:
	s_barrier
	s_add_i32 s77, s77, 1
	v_subrev_u32_e32 v215, 64, v215
	v_lshl_add_u64 v[194:195], v[194:195], 0, s[88:89]
	v_lshl_add_u64 v[196:197], v[196:197], 0, s[68:69]
	v_lshl_add_u64 v[198:199], v[198:199], 0, s[68:69]
	s_branch .Lm_E2

.Lm_t43_end:
	s_add_i32 s77, s77, 1
	v_subrev_u32_e32 v215, 64, v215
	s_cmp_ge_u32 s77, s42
	s_cbranch_scc1 .Lm_m44_slow
	s_cmp_le_u32 s77, s43
	s_cbranch_scc1 .Lm_nm45
	v_add_u32_e32 v239, 64, v215
	v_cmp_gt_i32_e64 s[4:5], 0, v239
	v_cmp_gt_i32_e64 s[6:7], 1, v239
	v_cmp_gt_i32_e64 s[8:9], 2, v239
	v_cmp_gt_i32_e64 s[10:11], 3, v239
	v_cndmask_b32_e64 v68, v68, v211, s[4:5]
	v_cndmask_b32_e64 v69, v69, v211, s[6:7]
	v_cndmask_b32_e64 v70, v70, v211, s[8:9]
	v_cndmask_b32_e64 v71, v71, v211, s[10:11]
	v_cmp_gt_i32_e64 s[4:5], 8, v239
	v_cmp_gt_i32_e64 s[6:7], 9, v239
	v_cmp_gt_i32_e64 s[8:9], 10, v239
	v_cmp_gt_i32_e64 s[10:11], 11, v239
	v_cndmask_b32_e64 v72, v72, v211, s[4:5]
	v_cndmask_b32_e64 v73, v73, v211, s[6:7]
	v_cndmask_b32_e64 v74, v74, v211, s[8:9]
	v_cndmask_b32_e64 v75, v75, v211, s[10:11]
	v_cmp_gt_i32_e64 s[4:5], 16, v239
	v_cmp_gt_i32_e64 s[6:7], 17, v239
	v_cmp_gt_i32_e64 s[8:9], 18, v239
	v_cmp_gt_i32_e64 s[10:11], 19, v239
	v_cndmask_b32_e64 v76, v76, v211, s[4:5]
	v_cndmask_b32_e64 v77, v77, v211, s[6:7]
	v_cndmask_b32_e64 v78, v78, v211, s[8:9]
	v_cndmask_b32_e64 v79, v79, v211, s[10:11]
	v_cmp_gt_i32_e64 s[4:5], 24, v239
	v_cmp_gt_i32_e64 s[6:7], 25, v239
	v_cmp_gt_i32_e64 s[8:9], 26, v239
	v_cmp_gt_i32_e64 s[10:11], 27, v239
	v_cndmask_b32_e64 v80, v80, v211, s[4:5]
	v_cndmask_b32_e64 v81, v81, v211, s[6:7]
	v_cndmask_b32_e64 v82, v82, v211, s[8:9]
	v_cndmask_b32_e64 v83, v83, v211, s[10:11]
	v_cmp_gt_i32_e64 s[4:5], 32, v239
	v_cmp_gt_i32_e64 s[6:7], 33, v239
	v_cmp_gt_i32_e64 s[8:9], 34, v239
	v_cmp_gt_i32_e64 s[10:11], 35, v239
	v_cndmask_b32_e64 v84, v84, v211, s[4:5]
	v_cndmask_b32_e64 v85, v85, v211, s[6:7]
	v_cndmask_b32_e64 v86, v86, v211, s[8:9]
	v_cndmask_b32_e64 v87, v87, v211, s[10:11]
	v_cmp_gt_i32_e64 s[4:5], 40, v239
	v_cmp_gt_i32_e64 s[6:7], 41, v239
	v_cmp_gt_i32_e64 s[8:9], 42, v239
	v_cmp_gt_i32_e64 s[10:11], 43, v239
	v_cndmask_b32_e64 v88, v88, v211, s[4:5]
	v_cndmask_b32_e64 v89, v89, v211, s[6:7]
	v_cndmask_b32_e64 v90, v90, v211, s[8:9]
	v_cndmask_b32_e64 v91, v91, v211, s[10:11]
	v_cmp_gt_i32_e64 s[4:5], 48, v239
	v_cmp_gt_i32_e64 s[6:7], 49, v239
	v_cmp_gt_i32_e64 s[8:9], 50, v239
	v_cmp_gt_i32_e64 s[10:11], 51, v239
	v_cndmask_b32_e64 v92, v92, v211, s[4:5]
	v_cndmask_b32_e64 v93, v93, v211, s[6:7]
	v_cndmask_b32_e64 v94, v94, v211, s[8:9]
	v_cndmask_b32_e64 v95, v95, v211, s[10:11]
	v_cmp_gt_i32_e64 s[4:5], 56, v239
	v_cmp_gt_i32_e64 s[6:7], 57, v239
	v_cmp_gt_i32_e64 s[8:9], 58, v239
	v_cmp_gt_i32_e64 s[10:11], 59, v239
	v_cndmask_b32_e64 v96, v96, v211, s[4:5]
	v_cndmask_b32_e64 v97, v97, v211, s[6:7]
	v_cndmask_b32_e64 v98, v98, v211, s[8:9]
	v_cndmask_b32_e64 v99, v99, v211, s[10:11]

.Lm_nd59:
	s_sub_i32 s5, s77, 2
	s_cmp_ge_u32 s5, s42
	s_cbranch_scc1 .Lm_t60_end
	v_add_f32_e32 v192, v68, v70
	v_add_f32_e32 v193, v69, v71
	v_add_f32_e32 v234, v84, v86
	v_add_f32_e32 v235, v85, v87
	v_add_f32_e32 v192, v72, v192
	v_add_f32_e32 v193, v73, v193
	v_cvt_pk_fp8_f32 v248, v68, v69
	v_add_f32_e32 v234, v88, v234
	v_add_f32_e32 v235, v89, v235
	v_cvt_pk_fp8_f32 v249, v72, v73
	v_add_f32_e32 v192, v74, v192
	v_add_f32_e32 v193, v75, v193
	v_cvt_pk_fp8_f32 v250, v76, v77
	v_add_f32_e32 v234, v90, v234
	v_add_f32_e32 v235, v91, v235
	v_cvt_pk_fp8_f32 v251, v80, v81
	v_add_f32_e32 v192, v76, v192
	v_add_f32_e32 v193, v77, v193
	v_cvt_pk_fp8_f32 v252, v84, v85
	v_add_f32_e32 v234, v92, v234
	v_add_f32_e32 v235, v93, v235
	v_cvt_pk_fp8_f32 v253, v88, v89
	v_add_f32_e32 v192, v78, v192
	v_add_f32_e32 v193, v79, v193
	v_cvt_pk_fp8_f32 v254, v92, v93
	v_add_f32_e32 v234, v94, v234
	v_add_f32_e32 v235, v95, v235
	v_cvt_pk_fp8_f32 v255, v96, v97
	v_add_f32_e32 v192, v80, v192
	v_add_f32_e32 v193, v81, v193
	v_add_f32_e32 v234, v96, v234
	v_add_f32_e32 v235, v97, v235
	v_add_f32_e32 v192, v82, v192
	v_add_f32_e32 v193, v83, v193
	v_add_f32_e32 v234, v98, v234
	v_add_f32_e32 v235, v99, v235
	v_add_f32_e32 v192, v192, v234
	v_add_f32_e32 v193, v193, v235
	v_cvt_pk_fp8_f32 v248, v70, v71 op_sel:[0,0,1]
	v_cvt_pk_fp8_f32 v249, v74, v75 op_sel:[0,0,1]
	v_cvt_pk_fp8_f32 v250, v78, v79 op_sel:[0,0,1]
	v_cvt_pk_fp8_f32 v251, v82, v83 op_sel:[0,0,1]
	v_add_f32_e32 v239, v192, v193
	v_cvt_pk_fp8_f32 v252, v86, v87 op_sel:[0,0,1]
	v_cvt_pk_fp8_f32 v253, v90, v91 op_sel:[0,0,1]
	v_mov_b32_e32 v235, v239
	v_cvt_pk_fp8_f32 v254, v94, v95 op_sel:[0,0,1]
	v_cvt_pk_fp8_f32 v255, v98, v99 op_sel:[0,0,1]
	v_permlane32_swap_b32_e32 v239, v235
	v_add_f32_e32 v239, v239, v235
	v_fma_f32 v2, v2, v217, v239
	v_mov_b32_e32 v217, 1.0

.Lm_nd67:
	s_sub_i32 s5, s77, 2
	s_cmp_ge_u32 s5, s42
	s_cbranch_scc1 .Lm_t68_end
	v_add_f32_e32 v192, v124, v126
	v_add_f32_e32 v193, v125, v127
	v_add_f32_e32 v234, v140, v142
	v_add_f32_e32 v235, v141, v143
	v_add_f32_e32 v192, v128, v192
	v_add_f32_e32 v193, v129, v193
	v_cvt_pk_fp8_f32 v248, v124, v125
	v_add_f32_e32 v234, v144, v234
	v_add_f32_e32 v235, v145, v235
	v_cvt_pk_fp8_f32 v249, v128, v129
	v_add_f32_e32 v192, v130, v192
	v_add_f32_e32 v193, v131, v193
	v_cvt_pk_fp8_f32 v250, v132, v133
	v_add_f32_e32 v234, v146, v234
	v_add_f32_e32 v235, v147, v235
	v_cvt_pk_fp8_f32 v251, v136, v137
	v_add_f32_e32 v192, v132, v192
	v_add_f32_e32 v193, v133, v193
	v_cvt_pk_fp8_f32 v252, v140, v141
	v_add_f32_e32 v234, v148, v234
	v_add_f32_e32 v235, v149, v235
	v_cvt_pk_fp8_f32 v253, v144, v145
	v_add_f32_e32 v192, v134, v192
	v_add_f32_e32 v193, v135, v193
	v_cvt_pk_fp8_f32 v254, v148, v149
	v_add_f32_e32 v234, v150, v234
	v_add_f32_e32 v235, v151, v235
	v_cvt_pk_fp8_f32 v255, v152, v153
	v_add_f32_e32 v192, v136, v192
	v_add_f32_e32 v193, v137, v193
	v_add_f32_e32 v234, v152, v234
	v_add_f32_e32 v235, v153, v235
	v_add_f32_e32 v192, v138, v192
	v_add_f32_e32 v193, v139, v193
	v_add_f32_e32 v234, v154, v234
	v_add_f32_e32 v235, v155, v235
	v_add_f32_e32 v192, v192, v234
	v_add_f32_e32 v193, v193, v235
	v_cvt_pk_fp8_f32 v248, v126, v127 op_sel:[0,0,1]
	v_cvt_pk_fp8_f32 v249, v130, v131 op_sel:[0,0,1]
	v_cvt_pk_fp8_f32 v250, v134, v135 op_sel:[0,0,1]
	v_cvt_pk_fp8_f32 v251, v138, v139 op_sel:[0,0,1]
	v_add_f32_e32 v239, v192, v193
	v_cvt_pk_fp8_f32 v252, v142, v143 op_sel:[0,0,1]
	v_cvt_pk_fp8_f32 v253, v146, v147 op_sel:[0,0,1]
	v_mov_b32_e32 v235, v239
	v_cvt_pk_fp8_f32 v254, v150, v151 op_sel:[0,0,1]
	v_cvt_pk_fp8_f32 v255, v154, v155 op_sel:[0,0,1]
	v_permlane32_swap_b32_e32 v239, v235
	v_add_f32_e32 v239, v239, v235
	v_fma_f32 v2, v2, v217, v239
	v_mov_b32_e32 v217, 1.0

.Lm_m83_end:
	s_waitcnt vmcnt(0) lgkmcnt(0)
	s_cmp_eq_u32 s48, 0
	s_cbranch_scc1 .Lm_bi86
	v_pk_mul_f32 v[226:227], v[226:227], s[50:51]
	v_pk_mul_f32 v[228:229], v[228:229], s[50:51]
	v_pk_mul_f32 v[230:231], v[230:231], s[50:51]
	v_pk_mul_f32 v[232:233], v[232:233], s[50:51]
	v_med3_f32 v226, v226, s33, v212
	v_med3_f32 v227, v227, s33, v212
	v_med3_f32 v228, v228, s33, v212
	v_med3_f32 v229, v229, s33, v212
	v_med3_f32 v230, v230, s33, v212
	v_med3_f32 v231, v231, s33, v212
	v_med3_f32 v232, v232, s33, v212
	v_med3_f32 v233, v233, s33, v212
	v_cvt_pk_fp8_f32 v244, v226, v227
	v_cvt_pk_fp8_f32 v245, v230, v231
	v_cvt_pk_fp8_f32 v244, v228, v229 op_sel:[0,0,1]
	v_cvt_pk_fp8_f32 v245, v232, v233 op_sel:[0,0,1]
	global_load_dword v226, v241, s[14:15]
	s_add_u32 s14, s14, s46
	s_addc_u32 s15, s15, 0
	global_load_dword v227, v241, s[14:15]
	s_add_u32 s14, s14, s46
	s_addc_u32 s15, s15, 0
	global_load_dword v228, v241, s[14:15]
	s_add_u32 s14, s14, s46
	s_addc_u32 s15, s15, 0
	global_load_dword v229, v241, s[14:15]
	s_add_u32 s14, s14, s46
	s_addc_u32 s15, s15, 0
	global_load_dword v230, v241, s[14:15]
	s_add_u32 s14, s14, s46
	s_addc_u32 s15, s15, 0
	global_load_dword v231, v241, s[14:15]
	s_add_u32 s14, s14, s46
	s_addc_u32 s15, s15, 0
	global_load_dword v232, v241, s[14:15]
	s_add_u32 s14, s14, s46
	s_addc_u32 s15, s15, 0
	global_load_dword v233, v241, s[14:15]
	s_add_u32 s14, s14, s46
	s_addc_u32 s15, s15, 0
.Lm_bi86:
	s_barrier
	s_add_i32 s77, s77, 1
	v_subrev_u32_e32 v215, 64, v215
	v_lshl_add_u64 v[194:195], v[194:195], 0, s[88:89]
	v_lshl_add_u64 v[196:197], v[196:197], 0, s[68:69]
	v_lshl_add_u64 v[198:199], v[198:199], 0, s[68:69]
	s_branch .Lm_L2

.Lm_m88_end:
	s_add_i32 s77, s77, 1
	v_subrev_u32_e32 v215, 64, v215
	s_sub_i32 s5, s77, 2
	s_cmp_ge_u32 s5, s42
	s_cbranch_scc1 .Lm_t91_end
	v_add_f32_e32 v192, v124, v126
	v_add_f32_e32 v193, v125, v127
	v_add_f32_e32 v234, v140, v142
	v_add_f32_e32 v235, v141, v143
	v_add_f32_e32 v192, v128, v192
	v_add_f32_e32 v193, v129, v193
	v_cvt_pk_fp8_f32 v248, v124, v125
	v_add_f32_e32 v234, v144, v234
	v_add_f32_e32 v235, v145, v235
	v_cvt_pk_fp8_f32 v249, v128, v129
	v_add_f32_e32 v192, v130, v192
	v_add_f32_e32 v193, v131, v193
	v_cvt_pk_fp8_f32 v250, v132, v133
	v_add_f32_e32 v234, v146, v234
	v_add_f32_e32 v235, v147, v235
	v_cvt_pk_fp8_f32 v251, v136, v137
	v_add_f32_e32 v192, v132, v192
	v_add_f32_e32 v193, v133, v193
	v_cvt_pk_fp8_f32 v252, v140, v141
	v_add_f32_e32 v234, v148, v234
	v_add_f32_e32 v235, v149, v235
	v_cvt_pk_fp8_f32 v253, v144, v145
	v_add_f32_e32 v192, v134, v192
	v_add_f32_e32 v193, v135, v193
	v_cvt_pk_fp8_f32 v254, v148, v149
	v_add_f32_e32 v234, v150, v234
	v_add_f32_e32 v235, v151, v235
	v_cvt_pk_fp8_f32 v255, v152, v153
	v_add_f32_e32 v192, v136, v192
	v_add_f32_e32 v193, v137, v193
	v_add_f32_e32 v234, v152, v234
	v_add_f32_e32 v235, v153, v235
	v_add_f32_e32 v192, v138, v192
	v_add_f32_e32 v193, v139, v193
	v_add_f32_e32 v234, v154, v234
	v_add_f32_e32 v235, v155, v235
	v_add_f32_e32 v192, v192, v234
	v_add_f32_e32 v193, v193, v235
	v_cvt_pk_fp8_f32 v248, v126, v127 op_sel:[0,0,1]
	v_cvt_pk_fp8_f32 v249, v130, v131 op_sel:[0,0,1]
	v_cvt_pk_fp8_f32 v250, v134, v135 op_sel:[0,0,1]
	v_cvt_pk_fp8_f32 v251, v138, v139 op_sel:[0,0,1]
	v_add_f32_e32 v239, v192, v193
	v_cvt_pk_fp8_f32 v252, v142, v143 op_sel:[0,0,1]
	v_cvt_pk_fp8_f32 v253, v146, v147 op_sel:[0,0,1]
	v_mov_b32_e32 v235, v239
	v_cvt_pk_fp8_f32 v254, v150, v151 op_sel:[0,0,1]
	v_cvt_pk_fp8_f32 v255, v154, v155 op_sel:[0,0,1]
	v_permlane32_swap_b32_e32 v239, v235
	v_add_f32_e32 v239, v239, v235
	v_fma_f32 v2, v2, v217, v239
	v_mov_b32_e32 v217, 1.0

.Lm_bf95:
	s_branch .Lm_exit
.Lm_m13_slow:
	s_cmp_lg_u32 s77, s42
	s_cbranch_scc1 .Lm_m13_s2
	s_cmp_le_u32 s77, s43
	s_cbranch_scc1 .Lm_nm96
	v_add_u32_e32 v239, 64, v215
	v_cmp_gt_i32_e64 s[4:5], 0, v239
	v_cmp_gt_i32_e64 s[6:7], 1, v239
	v_cmp_gt_i32_e64 s[8:9], 2, v239
	v_cmp_gt_i32_e64 s[10:11], 3, v239
	v_cndmask_b32_e64 v124, v124, v211, s[4:5]
	v_cndmask_b32_e64 v125, v125, v211, s[6:7]
	v_cndmask_b32_e64 v126, v126, v211, s[8:9]
	v_cndmask_b32_e64 v127, v127, v211, s[10:11]
	v_cmp_gt_i32_e64 s[4:5], 8, v239
	v_cmp_gt_i32_e64 s[6:7], 9, v239
	v_cmp_gt_i32_e64 s[8:9], 10, v239
	v_cmp_gt_i32_e64 s[10:11], 11, v239
	v_cndmask_b32_e64 v128, v128, v211, s[4:5]
	v_cndmask_b32_e64 v129, v129, v211, s[6:7]
	v_cndmask_b32_e64 v130, v130, v211, s[8:9]
	v_cndmask_b32_e64 v131, v131, v211, s[10:11]
	v_cmp_gt_i32_e64 s[4:5], 16, v239
	v_cmp_gt_i32_e64 s[6:7], 17, v239
	v_cmp_gt_i32_e64 s[8:9], 18, v239
	v_cmp_gt_i32_e64 s[10:11], 19, v239
	v_cndmask_b32_e64 v132, v132, v211, s[4:5]
	v_cndmask_b32_e64 v133, v133, v211, s[6:7]
	v_cndmask_b32_e64 v134, v134, v211, s[8:9]
	v_cndmask_b32_e64 v135, v135, v211, s[10:11]
	v_cmp_gt_i32_e64 s[4:5], 24, v239
	v_cmp_gt_i32_e64 s[6:7], 25, v239
	v_cmp_gt_i32_e64 s[8:9], 26, v239
	v_cmp_gt_i32_e64 s[10:11], 27, v239
	v_cndmask_b32_e64 v136, v136, v211, s[4:5]
	v_cndmask_b32_e64 v137, v137, v211, s[6:7]
	v_cndmask_b32_e64 v138, v138, v211, s[8:9]
	v_cndmask_b32_e64 v139, v139, v211, s[10:11]
	v_cmp_gt_i32_e64 s[4:5], 32, v239
	v_cmp_gt_i32_e64 s[6:7], 33, v239
	v_cmp_gt_i32_e64 s[8:9], 34, v239
	v_cmp_gt_i32_e64 s[10:11], 35, v239
	v_cndmask_b32_e64 v140, v140, v211, s[4:5]
	v_cndmask_b32_e64 v141, v141, v211, s[6:7]
	v_cndmask_b32_e64 v142, v142, v211, s[8:9]
	v_cndmask_b32_e64 v143, v143, v211, s[10:11]
	v_cmp_gt_i32_e64 s[4:5], 40, v239
	v_cmp_gt_i32_e64 s[6:7], 41, v239
	v_cmp_gt_i32_e64 s[8:9], 42, v239
	v_cmp_gt_i32_e64 s[10:11], 43, v239
	v_cndmask_b32_e64 v144, v144, v211, s[4:5]
	v_cndmask_b32_e64 v145, v145, v211, s[6:7]
	v_cndmask_b32_e64 v146, v146, v211, s[8:9]
	v_cndmask_b32_e64 v147, v147, v211, s[10:11]
	v_cmp_gt_i32_e64 s[4:5], 48, v239
	v_cmp_gt_i32_e64 s[6:7], 49, v239
	v_cmp_gt_i32_e64 s[8:9], 50, v239
	v_cmp_gt_i32_e64 s[10:11], 51, v239
	v_cndmask_b32_e64 v148, v148, v211, s[4:5]
	v_cndmask_b32_e64 v149, v149, v211, s[6:7]
	v_cndmask_b32_e64 v150, v150, v211, s[8:9]
	v_cndmask_b32_e64 v151, v151, v211, s[10:11]
	v_cmp_gt_i32_e64 s[4:5], 56, v239
	v_cmp_gt_i32_e64 s[6:7], 57, v239
	v_cmp_gt_i32_e64 s[8:9], 58, v239
	v_cmp_gt_i32_e64 s[10:11], 59, v239
	v_cndmask_b32_e64 v152, v152, v211, s[4:5]
	v_cndmask_b32_e64 v153, v153, v211, s[6:7]
	v_cndmask_b32_e64 v154, v154, v211, s[8:9]
	v_cndmask_b32_e64 v155, v155, v211, s[10:11]
.Lm_nm96:
	ds_read_b128 v[166:169], v207 offset:0
	ds_read_b128 v[170:173], v208 offset:0
	ds_read_b128 v[174:177], v207 offset:2048
	ds_read_b128 v[178:181], v208 offset:2048
	ds_read_b128 v[182:185], v207 offset:4096
	ds_read_b128 v[186:189], v208 offset:4096
	ds_read_b128 v[218:221], v207 offset:6144
	ds_read_b128 v[222:225], v208 offset:6144
	s_waitcnt lgkmcnt(6)
	v_mfma_f32_32x32x64_f8f6f4 v[52:67], v[248:255], v[166:173], v[52:67]
	s_waitcnt lgkmcnt(4)
	v_mfma_f32_32x32x64_f8f6f4 v[36:51], v[248:255], v[174:181], v[36:51]
	s_waitcnt lgkmcnt(2)
	v_mfma_f32_32x32x64_f8f6f4 v[20:35], v[248:255], v[182:189], v[20:35]
	s_waitcnt lgkmcnt(0)
	v_mfma_f32_32x32x64_f8f6f4 v[4:19], v[248:255], v[218:225], v[4:19]
	v_max3_f32 v239, v124, v125, v126
	v_max3_f32 v235, v140, v141, v142
	v_max3_f32 v239, v239, v127, v128
	v_max3_f32 v235, v235, v143, v144
	v_max3_f32 v239, v239, v129, v130
	v_max3_f32 v235, v235, v145, v146
	v_max3_f32 v239, v239, v131, v132
	v_max3_f32 v235, v235, v147, v148
	v_max3_f32 v239, v239, v133, v134
	v_max3_f32 v235, v235, v149, v150
	v_max3_f32 v239, v239, v135, v136
	v_max3_f32 v235, v235, v151, v152
	v_max3_f32 v239, v239, v137, v138
	v_max3_f32 v235, v235, v153, v154
	v_max3_f32 v239, v239, v139, v155
	v_max_f32_e32 v239, v239, v235
	v_mov_b32_e32 v234, v239
	s_nop 1
	v_permlane32_swap_b32_e32 v239, v234
	v_max_f32_e32 v239, v239, v234
	v_sub_f32_e32 v235, v239, v216
	v_mul_f32_e32 v235, 0x3a93cd3a, v235
	v_cmp_ge_f32_e32 vcc, 2.0, v235
	s_cmp_eq_u64 vcc, exec
	s_cbranch_scc1 .Lm_nr97
	v_max_f32_e32 v235, v216, v239
	v_sub_f32_e32 v217, v216, v235
	v_mul_f32_e32 v217, 0x3ad53b94, v217
	v_exp_f32_e32 v217, v217
	v_mov_b32_e32 v216, v235
	s_and_saveexec_b64 s[6:7], s[0:1]
	ds_write_b32 v214, v217 offset:128
	s_or_b64 exec, exec, s[6:7]
	s_waitcnt lgkmcnt(0)
	ds_read_b128 v[84:87], v213 offset:128
	s_waitcnt lgkmcnt(0)
	v_pk_mul_f32 v[52:53], v[52:53], v[84:85]
	v_pk_mul_f32 v[54:55], v[54:55], v[86:87]
	v_pk_mul_f32 v[36:37], v[36:37], v[84:85]
	v_pk_mul_f32 v[38:39], v[38:39], v[86:87]
	v_pk_mul_f32 v[20:21], v[20:21], v[84:85]
	v_pk_mul_f32 v[22:23], v[22:23], v[86:87]
	v_pk_mul_f32 v[4:5], v[4:5], v[84:85]
	v_pk_mul_f32 v[6:7], v[6:7], v[86:87]
	ds_read_b128 v[84:87], v213 offset:160
	s_waitcnt lgkmcnt(0)
	v_pk_mul_f32 v[56:57], v[56:57], v[84:85]
	v_pk_mul_f32 v[58:59], v[58:59], v[86:87]
	v_pk_mul_f32 v[40:41], v[40:41], v[84:85]
	v_pk_mul_f32 v[42:43], v[42:43], v[86:87]
	v_pk_mul_f32 v[24:25], v[24:25], v[84:85]
	v_pk_mul_f32 v[26:27], v[26:27], v[86:87]
	v_pk_mul_f32 v[8:9], v[8:9], v[84:85]
	v_pk_mul_f32 v[10:11], v[10:11], v[86:87]
	ds_read_b128 v[84:87], v213 offset:192
	s_waitcnt lgkmcnt(0)
	v_pk_mul_f32 v[60:61], v[60:61], v[84:85]
	v_pk_mul_f32 v[62:63], v[62:63], v[86:87]
	v_pk_mul_f32 v[44:45], v[44:45], v[84:85]
	v_pk_mul_f32 v[46:47], v[46:47], v[86:87]
	v_pk_mul_f32 v[28:29], v[28:29], v[84:85]
	v_pk_mul_f32 v[30:31], v[30:31], v[86:87]
	v_pk_mul_f32 v[12:13], v[12:13], v[84:85]
	v_pk_mul_f32 v[14:15], v[14:15], v[86:87]
	ds_read_b128 v[84:87], v213 offset:224
	s_waitcnt lgkmcnt(0)
	v_pk_mul_f32 v[64:65], v[64:65], v[84:85]
	v_pk_mul_f32 v[66:67], v[66:67], v[86:87]
	v_pk_mul_f32 v[48:49], v[48:49], v[84:85]
	v_pk_mul_f32 v[50:51], v[50:51], v[86:87]
	v_pk_mul_f32 v[32:33], v[32:33], v[84:85]
	v_pk_mul_f32 v[34:35], v[34:35], v[86:87]
	v_pk_mul_f32 v[16:17], v[16:17], v[84:85]
	v_pk_mul_f32 v[18:19], v[18:19], v[86:87]
.Lm_nr97:
	v_fmamk_f32 v190, v216, 0xbad53b94, v210
	v_fma_f32 v124, v124, s96, v190
	v_fma_f32 v125, v125, s96, v190
	v_fma_f32 v140, v140, s96, v190
	v_fma_f32 v141, v141, s96, v190
	v_fma_f32 v126, v126, s96, v190
	v_fma_f32 v127, v127, s96, v190
	v_fma_f32 v142, v142, s96, v190
	v_fma_f32 v143, v143, s96, v190
	v_fma_f32 v128, v128, s96, v190
	v_fma_f32 v129, v129, s96, v190
	v_fma_f32 v144, v144, s96, v190
	v_fma_f32 v145, v145, s96, v190
	v_fma_f32 v130, v130, s96, v190
	v_fma_f32 v131, v131, s96, v190
	v_fma_f32 v146, v146, s96, v190
	v_fma_f32 v147, v147, s96, v190
	v_fma_f32 v132, v132, s96, v190
	v_fma_f32 v133, v133, s96, v190
	v_fma_f32 v148, v148, s96, v190
	v_fma_f32 v149, v149, s96, v190
	v_fma_f32 v134, v134, s96, v190
	v_fma_f32 v135, v135, s96, v190
	v_fma_f32 v150, v150, s96, v190
	v_fma_f32 v151, v151, s96, v190
	v_fma_f32 v136, v136, s96, v190
	v_fma_f32 v137, v137, s96, v190
	v_fma_f32 v152, v152, s96, v190
	v_fma_f32 v153, v153, s96, v190
	v_fma_f32 v138, v138, s96, v190
	v_fma_f32 v139, v139, s96, v190
	v_fma_f32 v154, v154, s96, v190
	v_fma_f32 v155, v155, s96, v190
	v_exp_f32_e32 v124, v124
	v_exp_f32_e32 v125, v125
	v_exp_f32_e32 v126, v126
	v_exp_f32_e32 v127, v127
	v_exp_f32_e32 v128, v128
	v_exp_f32_e32 v129, v129
	v_exp_f32_e32 v130, v130
	v_exp_f32_e32 v131, v131
	v_exp_f32_e32 v132, v132
	v_exp_f32_e32 v133, v133
	v_exp_f32_e32 v134, v134
	v_exp_f32_e32 v135, v135
	v_exp_f32_e32 v136, v136
	v_exp_f32_e32 v137, v137
	v_exp_f32_e32 v138, v138
	v_exp_f32_e32 v139, v139
	v_exp_f32_e32 v140, v140
	v_exp_f32_e32 v141, v141
	v_exp_f32_e32 v142, v142
	v_exp_f32_e32 v143, v143
	v_exp_f32_e32 v144, v144
	v_exp_f32_e32 v145, v145
	v_exp_f32_e32 v146, v146
	v_exp_f32_e32 v147, v147
	v_exp_f32_e32 v148, v148
	v_exp_f32_e32 v149, v149
	v_exp_f32_e32 v150, v150
	v_exp_f32_e32 v151, v151
	v_exp_f32_e32 v152, v152
	v_exp_f32_e32 v153, v153
	v_exp_f32_e32 v154, v154
	v_exp_f32_e32 v155, v155
	s_branch .Lm_m13_end
.Lm_m13_s2:
	s_sub_i32 s5, s77, 1
	s_cmp_lg_u32 s5, s42
	s_cbranch_scc1 .Lm_m13_end
	ds_read_b128 v[166:169], v207 offset:0
	ds_read_b128 v[170:173], v208 offset:0
	ds_read_b128 v[174:177], v207 offset:2048
	ds_read_b128 v[178:181], v208 offset:2048
	ds_read_b128 v[182:185], v207 offset:4096
	ds_read_b128 v[186:189], v208 offset:4096
	ds_read_b128 v[218:221], v207 offset:6144
	ds_read_b128 v[222:225], v208 offset:6144
	s_waitcnt lgkmcnt(6)
	v_mfma_f32_32x32x64_f8f6f4 v[52:67], v[248:255], v[166:173], v[52:67]
	s_waitcnt lgkmcnt(4)
	v_mfma_f32_32x32x64_f8f6f4 v[36:51], v[248:255], v[174:181], v[36:51]
	s_waitcnt lgkmcnt(2)
	v_mfma_f32_32x32x64_f8f6f4 v[20:35], v[248:255], v[182:189], v[20:35]
	s_waitcnt lgkmcnt(0)
	v_mfma_f32_32x32x64_f8f6f4 v[4:19], v[248:255], v[218:225], v[4:19]
	s_branch .Lm_m13_end

.Lm_nm98:
	ds_read_b128 v[166:169], v207 offset:16384
	ds_read_b128 v[170:173], v208 offset:16384
	ds_read_b128 v[174:177], v207 offset:18432
	ds_read_b128 v[178:181], v208 offset:18432
	ds_read_b128 v[182:185], v207 offset:20480
	ds_read_b128 v[186:189], v208 offset:20480
	ds_read_b128 v[218:221], v207 offset:22528
	ds_read_b128 v[222:225], v208 offset:22528
	s_waitcnt lgkmcnt(6)
	v_mfma_f32_32x32x64_f8f6f4 v[52:67], v[248:255], v[166:173], v[52:67]
	s_waitcnt lgkmcnt(4)
	v_mfma_f32_32x32x64_f8f6f4 v[36:51], v[248:255], v[174:181], v[36:51]
	s_waitcnt lgkmcnt(2)
	v_mfma_f32_32x32x64_f8f6f4 v[20:35], v[248:255], v[182:189], v[20:35]
	s_waitcnt lgkmcnt(0)
	v_mfma_f32_32x32x64_f8f6f4 v[4:19], v[248:255], v[218:225], v[4:19]
	v_max3_f32 v239, v68, v69, v70
	v_max3_f32 v235, v84, v85, v86
	v_max3_f32 v239, v239, v71, v72
	v_max3_f32 v235, v235, v87, v88
	v_max3_f32 v239, v239, v73, v74
	v_max3_f32 v235, v235, v89, v90
	v_max3_f32 v239, v239, v75, v76
	v_max3_f32 v235, v235, v91, v92
	v_max3_f32 v239, v239, v77, v78
	v_max3_f32 v235, v235, v93, v94
	v_max3_f32 v239, v239, v79, v80
	v_max3_f32 v235, v235, v95, v96
	v_max3_f32 v239, v239, v81, v82
	v_max3_f32 v235, v235, v97, v98
	v_max3_f32 v239, v239, v83, v99
	v_max_f32_e32 v239, v239, v235
	v_mov_b32_e32 v234, v239
	s_nop 1
	v_permlane32_swap_b32_e32 v239, v234
	v_max_f32_e32 v239, v239, v234
	v_sub_f32_e32 v235, v239, v216
	v_mul_f32_e32 v235, 0x3a93cd3a, v235
	v_cmp_ge_f32_e32 vcc, 2.0, v235
	s_cmp_eq_u64 vcc, exec
	s_cbranch_scc1 .Lm_nr99
	v_max_f32_e32 v235, v216, v239
	v_sub_f32_e32 v217, v216, v235
	v_mul_f32_e32 v217, 0x3ad53b94, v217
	v_exp_f32_e32 v217, v217
	v_mov_b32_e32 v216, v235
	s_and_saveexec_b64 s[6:7], s[0:1]
	ds_write_b32 v214, v217 offset:128
	s_or_b64 exec, exec, s[6:7]
	s_waitcnt lgkmcnt(0)
	ds_read_b128 v[140:143], v213 offset:128
	s_waitcnt lgkmcnt(0)
	v_pk_mul_f32 v[52:53], v[52:53], v[140:141]
	v_pk_mul_f32 v[54:55], v[54:55], v[142:143]
	v_pk_mul_f32 v[36:37], v[36:37], v[140:141]
	v_pk_mul_f32 v[38:39], v[38:39], v[142:143]
	v_pk_mul_f32 v[20:21], v[20:21], v[140:141]
	v_pk_mul_f32 v[22:23], v[22:23], v[142:143]
	v_pk_mul_f32 v[4:5], v[4:5], v[140:141]
	v_pk_mul_f32 v[6:7], v[6:7], v[142:143]
	ds_read_b128 v[140:143], v213 offset:160
	s_waitcnt lgkmcnt(0)
	v_pk_mul_f32 v[56:57], v[56:57], v[140:141]
	v_pk_mul_f32 v[58:59], v[58:59], v[142:143]
	v_pk_mul_f32 v[40:41], v[40:41], v[140:141]
	v_pk_mul_f32 v[42:43], v[42:43], v[142:143]
	v_pk_mul_f32 v[24:25], v[24:25], v[140:141]
	v_pk_mul_f32 v[26:27], v[26:27], v[142:143]
	v_pk_mul_f32 v[8:9], v[8:9], v[140:141]
	v_pk_mul_f32 v[10:11], v[10:11], v[142:143]
	ds_read_b128 v[140:143], v213 offset:192
	s_waitcnt lgkmcnt(0)
	v_pk_mul_f32 v[60:61], v[60:61], v[140:141]
	v_pk_mul_f32 v[62:63], v[62:63], v[142:143]
	v_pk_mul_f32 v[44:45], v[44:45], v[140:141]
	v_pk_mul_f32 v[46:47], v[46:47], v[142:143]
	v_pk_mul_f32 v[28:29], v[28:29], v[140:141]
	v_pk_mul_f32 v[30:31], v[30:31], v[142:143]
	v_pk_mul_f32 v[12:13], v[12:13], v[140:141]
	v_pk_mul_f32 v[14:15], v[14:15], v[142:143]
	ds_read_b128 v[140:143], v213 offset:224
	s_waitcnt lgkmcnt(0)
	v_pk_mul_f32 v[64:65], v[64:65], v[140:141]
	v_pk_mul_f32 v[66:67], v[66:67], v[142:143]
	v_pk_mul_f32 v[48:49], v[48:49], v[140:141]
	v_pk_mul_f32 v[50:51], v[50:51], v[142:143]
	v_pk_mul_f32 v[32:33], v[32:33], v[140:141]
	v_pk_mul_f32 v[34:35], v[34:35], v[142:143]
	v_pk_mul_f32 v[16:17], v[16:17], v[140:141]
	v_pk_mul_f32 v[18:19], v[18:19], v[142:143]
.Lm_nr99:
	v_fmamk_f32 v190, v216, 0xbad53b94, v210
	v_fma_f32 v68, v68, s96, v190
	v_fma_f32 v69, v69, s96, v190
	v_fma_f32 v84, v84, s96, v190
	v_fma_f32 v85, v85, s96, v190
	v_fma_f32 v70, v70, s96, v190
	v_fma_f32 v71, v71, s96, v190
	v_fma_f32 v86, v86, s96, v190
	v_fma_f32 v87, v87, s96, v190
	v_fma_f32 v72, v72, s96, v190
	v_fma_f32 v73, v73, s96, v190
	v_fma_f32 v88, v88, s96, v190
	v_fma_f32 v89, v89, s96, v190
	v_fma_f32 v74, v74, s96, v190
	v_fma_f32 v75, v75, s96, v190
	v_fma_f32 v90, v90, s96, v190
	v_fma_f32 v91, v91, s96, v190
	v_fma_f32 v76, v76, s96, v190
	v_fma_f32 v77, v77, s96, v190
	v_fma_f32 v92, v92, s96, v190
	v_fma_f32 v93, v93, s96, v190
	v_fma_f32 v78, v78, s96, v190
	v_fma_f32 v79, v79, s96, v190
	v_fma_f32 v94, v94, s96, v190
	v_fma_f32 v95, v95, s96, v190
	v_fma_f32 v80, v80, s96, v190
	v_fma_f32 v81, v81, s96, v190
	v_fma_f32 v96, v96, s96, v190
	v_fma_f32 v97, v97, s96, v190
	v_fma_f32 v82, v82, s96, v190
	v_fma_f32 v83, v83, s96, v190
	v_fma_f32 v98, v98, s96, v190
	v_fma_f32 v99, v99, s96, v190
	v_exp_f32_e32 v68, v68
	v_exp_f32_e32 v69, v69
	v_exp_f32_e32 v70, v70
	v_exp_f32_e32 v71, v71
	v_exp_f32_e32 v72, v72
	v_exp_f32_e32 v73, v73
	v_exp_f32_e32 v74, v74
	v_exp_f32_e32 v75, v75
	v_exp_f32_e32 v76, v76
	v_exp_f32_e32 v77, v77
	v_exp_f32_e32 v78, v78
	v_exp_f32_e32 v79, v79
	v_exp_f32_e32 v80, v80
	v_exp_f32_e32 v81, v81
	v_exp_f32_e32 v82, v82
	v_exp_f32_e32 v83, v83
	v_exp_f32_e32 v84, v84
	v_exp_f32_e32 v85, v85
	v_exp_f32_e32 v86, v86
	v_exp_f32_e32 v87, v87
	v_exp_f32_e32 v88, v88
	v_exp_f32_e32 v89, v89
	v_exp_f32_e32 v90, v90
	v_exp_f32_e32 v91, v91
	v_exp_f32_e32 v92, v92
	v_exp_f32_e32 v93, v93
	v_exp_f32_e32 v94, v94
	v_exp_f32_e32 v95, v95
	v_exp_f32_e32 v96, v96
	v_exp_f32_e32 v97, v97
	v_exp_f32_e32 v98, v98
	v_exp_f32_e32 v99, v99
	s_branch .Lm_m21_end
.Lm_m21_s2:
	s_sub_i32 s5, s77, 1
	s_cmp_lg_u32 s5, s42
	s_cbranch_scc1 .Lm_m21_end
	ds_read_b128 v[166:169], v207 offset:16384
	ds_read_b128 v[170:173], v208 offset:16384
	ds_read_b128 v[174:177], v207 offset:18432
	ds_read_b128 v[178:181], v208 offset:18432
	ds_read_b128 v[182:185], v207 offset:20480
	ds_read_b128 v[186:189], v208 offset:20480
	ds_read_b128 v[218:221], v207 offset:22528
	ds_read_b128 v[222:225], v208 offset:22528
	s_waitcnt lgkmcnt(6)
	v_mfma_f32_32x32x64_f8f6f4 v[52:67], v[248:255], v[166:173], v[52:67]
	s_waitcnt lgkmcnt(4)
	v_mfma_f32_32x32x64_f8f6f4 v[36:51], v[248:255], v[174:181], v[36:51]
	s_waitcnt lgkmcnt(2)
	v_mfma_f32_32x32x64_f8f6f4 v[20:35], v[248:255], v[182:189], v[20:35]
	s_waitcnt lgkmcnt(0)
	v_mfma_f32_32x32x64_f8f6f4 v[4:19], v[248:255], v[218:225], v[4:19]
	s_branch .Lm_m21_end

.Lm_nm100:
	ds_read_b128 v[166:169], v207 offset:8192
	ds_read_b128 v[170:173], v208 offset:8192
	ds_read_b128 v[174:177], v207 offset:10240
	ds_read_b128 v[178:181], v208 offset:10240
	ds_read_b128 v[182:185], v207 offset:12288
	ds_read_b128 v[186:189], v208 offset:12288
	ds_read_b128 v[218:221], v207 offset:14336
	ds_read_b128 v[222:225], v208 offset:14336
	s_waitcnt lgkmcnt(6)
	v_mfma_f32_32x32x64_f8f6f4 v[52:67], v[248:255], v[166:173], v[52:67]
	s_waitcnt lgkmcnt(4)
	v_mfma_f32_32x32x64_f8f6f4 v[36:51], v[248:255], v[174:181], v[36:51]
	s_waitcnt lgkmcnt(2)
	v_mfma_f32_32x32x64_f8f6f4 v[20:35], v[248:255], v[182:189], v[20:35]
	s_waitcnt lgkmcnt(0)
	v_mfma_f32_32x32x64_f8f6f4 v[4:19], v[248:255], v[218:225], v[4:19]
	v_max3_f32 v239, v124, v125, v126
	v_max3_f32 v235, v140, v141, v142
	v_max3_f32 v239, v239, v127, v128
	v_max3_f32 v235, v235, v143, v144
	v_max3_f32 v239, v239, v129, v130
	v_max3_f32 v235, v235, v145, v146
	v_max3_f32 v239, v239, v131, v132
	v_max3_f32 v235, v235, v147, v148
	v_max3_f32 v239, v239, v133, v134
	v_max3_f32 v235, v235, v149, v150
	v_max3_f32 v239, v239, v135, v136
	v_max3_f32 v235, v235, v151, v152
	v_max3_f32 v239, v239, v137, v138
	v_max3_f32 v235, v235, v153, v154
	v_max3_f32 v239, v239, v139, v155
	v_max_f32_e32 v239, v239, v235
	v_mov_b32_e32 v234, v239
	s_nop 1
	v_permlane32_swap_b32_e32 v239, v234
	v_max_f32_e32 v239, v239, v234
	v_sub_f32_e32 v235, v239, v216
	v_mul_f32_e32 v235, 0x3a93cd3a, v235
	v_cmp_ge_f32_e32 vcc, 2.0, v235
	s_cmp_eq_u64 vcc, exec
	s_cbranch_scc1 .Lm_nr101
	v_max_f32_e32 v235, v216, v239
	v_sub_f32_e32 v217, v216, v235
	v_mul_f32_e32 v217, 0x3ad53b94, v217
	v_exp_f32_e32 v217, v217
	v_mov_b32_e32 v216, v235
	s_and_saveexec_b64 s[6:7], s[0:1]
	ds_write_b32 v214, v217 offset:128
	s_or_b64 exec, exec, s[6:7]
	s_waitcnt lgkmcnt(0)
	ds_read_b128 v[84:87], v213 offset:128
	s_waitcnt lgkmcnt(0)
	v_pk_mul_f32 v[52:53], v[52:53], v[84:85]
	v_pk_mul_f32 v[54:55], v[54:55], v[86:87]
	v_pk_mul_f32 v[36:37], v[36:37], v[84:85]
	v_pk_mul_f32 v[38:39], v[38:39], v[86:87]
	v_pk_mul_f32 v[20:21], v[20:21], v[84:85]
	v_pk_mul_f32 v[22:23], v[22:23], v[86:87]
	v_pk_mul_f32 v[4:5], v[4:5], v[84:85]
	v_pk_mul_f32 v[6:7], v[6:7], v[86:87]
	ds_read_b128 v[84:87], v213 offset:160
	s_waitcnt lgkmcnt(0)
	v_pk_mul_f32 v[56:57], v[56:57], v[84:85]
	v_pk_mul_f32 v[58:59], v[58:59], v[86:87]
	v_pk_mul_f32 v[40:41], v[40:41], v[84:85]
	v_pk_mul_f32 v[42:43], v[42:43], v[86:87]
	v_pk_mul_f32 v[24:25], v[24:25], v[84:85]
	v_pk_mul_f32 v[26:27], v[26:27], v[86:87]
	v_pk_mul_f32 v[8:9], v[8:9], v[84:85]
	v_pk_mul_f32 v[10:11], v[10:11], v[86:87]
	ds_read_b128 v[84:87], v213 offset:192
	s_waitcnt lgkmcnt(0)
	v_pk_mul_f32 v[60:61], v[60:61], v[84:85]
	v_pk_mul_f32 v[62:63], v[62:63], v[86:87]
	v_pk_mul_f32 v[44:45], v[44:45], v[84:85]
	v_pk_mul_f32 v[46:47], v[46:47], v[86:87]
	v_pk_mul_f32 v[28:29], v[28:29], v[84:85]
	v_pk_mul_f32 v[30:31], v[30:31], v[86:87]
	v_pk_mul_f32 v[12:13], v[12:13], v[84:85]
	v_pk_mul_f32 v[14:15], v[14:15], v[86:87]
	ds_read_b128 v[84:87], v213 offset:224
	s_waitcnt lgkmcnt(0)
	v_pk_mul_f32 v[64:65], v[64:65], v[84:85]
	v_pk_mul_f32 v[66:67], v[66:67], v[86:87]
	v_pk_mul_f32 v[48:49], v[48:49], v[84:85]
	v_pk_mul_f32 v[50:51], v[50:51], v[86:87]
	v_pk_mul_f32 v[32:33], v[32:33], v[84:85]
	v_pk_mul_f32 v[34:35], v[34:35], v[86:87]
	v_pk_mul_f32 v[16:17], v[16:17], v[84:85]
	v_pk_mul_f32 v[18:19], v[18:19], v[86:87]

.Lm_m27_s2:
	s_sub_i32 s5, s77, 1
	s_cmp_lg_u32 s5, s42
	s_cbranch_scc1 .Lm_m27_end
	ds_read_b128 v[166:169], v207 offset:8192
	ds_read_b128 v[170:173], v208 offset:8192
	ds_read_b128 v[174:177], v207 offset:10240
	ds_read_b128 v[178:181], v208 offset:10240
	ds_read_b128 v[182:185], v207 offset:12288
	ds_read_b128 v[186:189], v208 offset:12288
	ds_read_b128 v[218:221], v207 offset:14336
	ds_read_b128 v[222:225], v208 offset:14336
	s_waitcnt lgkmcnt(6)
	v_mfma_f32_32x32x64_f8f6f4 v[52:67], v[248:255], v[166:173], v[52:67]
	s_waitcnt lgkmcnt(4)
	v_mfma_f32_32x32x64_f8f6f4 v[36:51], v[248:255], v[174:181], v[36:51]
	s_waitcnt lgkmcnt(2)
	v_mfma_f32_32x32x64_f8f6f4 v[20:35], v[248:255], v[182:189], v[20:35]
	s_waitcnt lgkmcnt(0)
	v_mfma_f32_32x32x64_f8f6f4 v[4:19], v[248:255], v[218:225], v[4:19]
	s_branch .Lm_m27_end

.Lm_nm102:
	ds_read_b128 v[166:169], v207 offset:24576
	ds_read_b128 v[170:173], v208 offset:24576
	ds_read_b128 v[174:177], v207 offset:26624
	ds_read_b128 v[178:181], v208 offset:26624
	ds_read_b128 v[182:185], v207 offset:28672
	ds_read_b128 v[186:189], v208 offset:28672
	ds_read_b128 v[218:221], v207 offset:30720
	ds_read_b128 v[222:225], v208 offset:30720
	s_waitcnt lgkmcnt(6)
	v_mfma_f32_32x32x64_f8f6f4 v[52:67], v[248:255], v[166:173], v[52:67]
	s_waitcnt lgkmcnt(4)
	v_mfma_f32_32x32x64_f8f6f4 v[36:51], v[248:255], v[174:181], v[36:51]
	s_waitcnt lgkmcnt(2)
	v_mfma_f32_32x32x64_f8f6f4 v[20:35], v[248:255], v[182:189], v[20:35]
	s_waitcnt lgkmcnt(0)
	v_mfma_f32_32x32x64_f8f6f4 v[4:19], v[248:255], v[218:225], v[4:19]
	v_max3_f32 v239, v68, v69, v70
	v_max3_f32 v235, v84, v85, v86
	v_max3_f32 v239, v239, v71, v72
	v_max3_f32 v235, v235, v87, v88
	v_max3_f32 v239, v239, v73, v74
	v_max3_f32 v235, v235, v89, v90
	v_max3_f32 v239, v239, v75, v76
	v_max3_f32 v235, v235, v91, v92
	v_max3_f32 v239, v239, v77, v78
	v_max3_f32 v235, v235, v93, v94
	v_max3_f32 v239, v239, v79, v80
	v_max3_f32 v235, v235, v95, v96
	v_max3_f32 v239, v239, v81, v82
	v_max3_f32 v235, v235, v97, v98
	v_max3_f32 v239, v239, v83, v99
	v_max_f32_e32 v239, v239, v235
	v_mov_b32_e32 v234, v239
	s_nop 1
	v_permlane32_swap_b32_e32 v239, v234
	v_max_f32_e32 v239, v239, v234
	v_sub_f32_e32 v235, v239, v216
	v_mul_f32_e32 v235, 0x3a93cd3a, v235
	v_cmp_ge_f32_e32 vcc, 2.0, v235
	s_cmp_eq_u64 vcc, exec
	s_cbranch_scc1 .Lm_nr103
	v_max_f32_e32 v235, v216, v239
	v_sub_f32_e32 v217, v216, v235
	v_mul_f32_e32 v217, 0x3ad53b94, v217
	v_exp_f32_e32 v217, v217
	v_mov_b32_e32 v216, v235
	s_and_saveexec_b64 s[6:7], s[0:1]
	ds_write_b32 v214, v217 offset:128
	s_or_b64 exec, exec, s[6:7]
	s_waitcnt lgkmcnt(0)
	ds_read_b128 v[140:143], v213 offset:128
	s_waitcnt lgkmcnt(0)
	v_pk_mul_f32 v[52:53], v[52:53], v[140:141]
	v_pk_mul_f32 v[54:55], v[54:55], v[142:143]
	v_pk_mul_f32 v[36:37], v[36:37], v[140:141]
	v_pk_mul_f32 v[38:39], v[38:39], v[142:143]
	v_pk_mul_f32 v[20:21], v[20:21], v[140:141]
	v_pk_mul_f32 v[22:23], v[22:23], v[142:143]
	v_pk_mul_f32 v[4:5], v[4:5], v[140:141]
	v_pk_mul_f32 v[6:7], v[6:7], v[142:143]
	ds_read_b128 v[140:143], v213 offset:160
	s_waitcnt lgkmcnt(0)
	v_pk_mul_f32 v[56:57], v[56:57], v[140:141]
	v_pk_mul_f32 v[58:59], v[58:59], v[142:143]
	v_pk_mul_f32 v[40:41], v[40:41], v[140:141]
	v_pk_mul_f32 v[42:43], v[42:43], v[142:143]
	v_pk_mul_f32 v[24:25], v[24:25], v[140:141]
	v_pk_mul_f32 v[26:27], v[26:27], v[142:143]
	v_pk_mul_f32 v[8:9], v[8:9], v[140:141]
	v_pk_mul_f32 v[10:11], v[10:11], v[142:143]
	ds_read_b128 v[140:143], v213 offset:192
	s_waitcnt lgkmcnt(0)
	v_pk_mul_f32 v[60:61], v[60:61], v[140:141]
	v_pk_mul_f32 v[62:63], v[62:63], v[142:143]
	v_pk_mul_f32 v[44:45], v[44:45], v[140:141]
	v_pk_mul_f32 v[46:47], v[46:47], v[142:143]
	v_pk_mul_f32 v[28:29], v[28:29], v[140:141]
	v_pk_mul_f32 v[30:31], v[30:31], v[142:143]
	v_pk_mul_f32 v[12:13], v[12:13], v[140:141]
	v_pk_mul_f32 v[14:15], v[14:15], v[142:143]
	ds_read_b128 v[140:143], v213 offset:224
	s_waitcnt lgkmcnt(0)
	v_pk_mul_f32 v[64:65], v[64:65], v[140:141]
	v_pk_mul_f32 v[66:67], v[66:67], v[142:143]
	v_pk_mul_f32 v[48:49], v[48:49], v[140:141]
	v_pk_mul_f32 v[50:51], v[50:51], v[142:143]
	v_pk_mul_f32 v[32:33], v[32:33], v[140:141]
	v_pk_mul_f32 v[34:35], v[34:35], v[142:143]
	v_pk_mul_f32 v[16:17], v[16:17], v[140:141]
	v_pk_mul_f32 v[18:19], v[18:19], v[142:143]

.Lm_m35_s2:
	s_sub_i32 s5, s77, 1
	s_cmp_lg_u32 s5, s42
	s_cbranch_scc1 .Lm_m35_end
	ds_read_b128 v[166:169], v207 offset:24576
	ds_read_b128 v[170:173], v208 offset:24576
	ds_read_b128 v[174:177], v207 offset:26624
	ds_read_b128 v[178:181], v208 offset:26624
	ds_read_b128 v[182:185], v207 offset:28672
	ds_read_b128 v[186:189], v208 offset:28672
	ds_read_b128 v[218:221], v207 offset:30720
	ds_read_b128 v[222:225], v208 offset:30720
	s_waitcnt lgkmcnt(6)
	v_mfma_f32_32x32x64_f8f6f4 v[52:67], v[248:255], v[166:173], v[52:67]
	s_waitcnt lgkmcnt(4)
	v_mfma_f32_32x32x64_f8f6f4 v[36:51], v[248:255], v[174:181], v[36:51]
	s_waitcnt lgkmcnt(2)
	v_mfma_f32_32x32x64_f8f6f4 v[20:35], v[248:255], v[182:189], v[20:35]
	s_waitcnt lgkmcnt(0)
	v_mfma_f32_32x32x64_f8f6f4 v[4:19], v[248:255], v[218:225], v[4:19]
	s_branch .Lm_m35_end
